# GEMM k-loops: loop-top scalar address block moved behind the phase's LDS reads; 20 redundant post-barrier lgkmcnt(0) removed
# baseline (speedup 1.0000x reference)
; #define PG8_STAGE(bufoff, gbase, voff) do { _Pragma("unroll") for (int _i = 0; _i < 2; ++_i) \
;         __builtin_amdgcn_global_load_lds((const unsigned*)((const char*)(gbase) + (voff)[_i]), (LAS unsigned*)(lds + (bufoff) + ldsw + _i * 8192), 16, 0, 0); } while (0)
; #define PG8_LDA(dst, b, h) do { _Pragma("unroll") for (int m = 0; m < 4; ++m) _Pragma("unroll") for (int k = 0; k < 2; ++k) dst[m][k] = *(const LAS bf16x8*)(lds + PG8_SA(b, h) + aoff + m * 2048 + k * 1024); } while (0)
; #define PG8_LDB(dst, b, h) do { _Pragma("unroll") for (int n = 0; n < 2; ++n) _Pragma("unroll") for (int k = 0; k < 2; ++k) dst[n][k] = *(const LAS bf16x8*)(lds + PG8_SB(b, h) + boff + n * 2048 + k * 1024); } while (0)
; #define PG8_MMA(ai, bj, At, Bt) do { __builtin_amdgcn_s_setprio(1); _Pragma("unroll") for (int m = 0; m < 4; ++m) _Pragma("unroll") for (int n = 0; n < 2; ++n) _Pragma("unroll") for (int k = 0; k < 2; ++k) \
;         acc[ai][bj][m][n] = __builtin_amdgcn_mfma_f32_16x16x32_bf16(Bt[n][k], At[m][k], acc[ai][bj][m][n], 0, 0, 0); __builtin_amdgcn_s_setprio(0); } while (0)
; #define PG8_BAR __builtin_amdgcn_s_barrier()
; template <class Epi, class Sched, bool GATHER = false>
; __device__ __forceinline__ void gemm_phase(LAS unsigned char* lds, const int lda, const int ldb, const int K, const Sched& S, const Epi& E, const int* gidx = nullptr) {
;     ...
;             const char* a1 = cA + (size_t)(t + 1) * kstep;
;             const char* a2 = last ? nA : cA + (size_t)(t + 2) * kstep; const char* b2 = last ? nB : cB + (size_t)(t + 2) * kstep;
;             const char* a3 = a2 + kstep; const char* b3 = b2 + kstep;
;             unsigned o2[2][2];
; #pragma unroll
;             for (int hh = 0; hh < 2; ++hh)
; #pragma unroll
;                 for (int i = 0; i < 2; ++i) { if constexpr (GATHER) o2[hh][i] = last ? ofn[hh][i] : ofc[hh][i]; else o2[hh][i] = ofc[hh][i]; }
;             PG8_LDB(B0, 0, 0); PG8_LDB(B1, 0, 1); PG8_SCHED; PG8_LDA(At, 0, 0); PG8_STAGE(PG8_SA(1, 1), a1, ofc[1]);
;             PG8_WAIT_V(8); PG8_WAIT_L(0); PG8_BAR; PG8_MMA(0, 0, At, B0); PG8_MMA(0, 1, At, B1); PG8_BAR; PG8_SCHED;
;             PG8_LDA(At, 0, 1); PG8_STAGE(PG8_SB(0, 0), b2, voffB); PG8_STAGE(PG8_SB(0, 1), b2 + hstepB, voffB); PG8_STAGE(PG8_SA(0, 0), a2, o2[0]);
;             PG8_WAIT_V(8); PG8_WAIT_L(0); PG8_BAR; PG8_MMA(1, 0, At, B0); PG8_MMA(1, 1, At, B1); PG8_BAR; PG8_SCHED;
.LBB0_428:
	s_add_i32 s28, 0, 0x10000
	s_add_i32 s33, 0, 0x14000
	v_add_u32_e32 v142, s28, v175
	v_add_u32_e32 v158, s33, v175
	ds_read_b128 v[126:129], v142
	ds_read_b128 v[130:133], v142 offset:1024
	ds_read_b128 v[138:141], v142 offset:2048
	ds_read_b128 v[142:145], v142 offset:3072
	ds_read_b128 v[146:149], v158
	ds_read_b128 v[150:153], v158 offset:1024
	ds_read_b128 v[154:157], v158 offset:2048
	ds_read_b128 v[158:161], v158 offset:3072
	v_lshl_add_u64 v[234:235], s[72:73], 0, v[180:181]
	s_add_i32 m0, s59, 0xc000
	ds_read_b128 v[182:185], v229
	ds_read_b128 v[186:189], v229 offset:1024
	ds_read_b128 v[190:193], v229 offset:2048
	ds_read_b128 v[196:199], v229 offset:3072
	ds_read_b128 v[200:203], v229 offset:4096
	ds_read_b128 v[204:207], v229 offset:5120
	ds_read_b128 v[208:211], v229 offset:6144
	ds_read_b128 v[230:233], v229 offset:7168
	s_add_u32 s12, s72, 0x80
	s_addc_u32 s13, s73, 0
	s_cmp_eq_u32 s75, 28
	s_cselect_b32 s67, s81, s13
	s_cselect_b32 s66, s80, s12
	s_cselect_b32 s13, s83, s74
	s_cselect_b32 s12, s82, s60
	global_load_lds_dwordx4 v[234:235], off
	v_lshl_add_u64 v[234:235], s[72:73], 0, v[178:179]
	s_add_i32 m0, s59, 0xe000
	s_nop 0
	global_load_lds_dwordx4 v[234:235], off
	s_waitcnt vmcnt(8)
	s_waitcnt lgkmcnt(0)
	s_barrier
	s_setprio 1
	v_mfma_f32_16x16x32_bf16 v[134:137], v[126:129], v[182:185], v[134:137]
	v_mfma_f32_16x16x32_bf16 v[122:125], v[138:141], v[182:185], v[122:125]
	v_mfma_f32_16x16x32_bf16 v[110:113], v[126:129], v[190:193], v[110:113]
	v_mfma_f32_16x16x32_bf16 v[106:109], v[138:141], v[190:193], v[106:109]
	v_mfma_f32_16x16x32_bf16 v[94:97], v[126:129], v[200:203], v[94:97]
	v_mfma_f32_16x16x32_bf16 v[90:93], v[138:141], v[200:203], v[90:93]
	v_mfma_f32_16x16x32_bf16 v[78:81], v[126:129], v[208:211], v[78:81]
	v_mfma_f32_16x16x32_bf16 v[74:77], v[138:141], v[208:211], v[74:77]
	v_mfma_f32_16x16x32_bf16 v[134:137], v[130:133], v[186:189], v[134:137]
	v_mfma_f32_16x16x32_bf16 v[122:125], v[142:145], v[186:189], v[122:125]
	v_mfma_f32_16x16x32_bf16 v[110:113], v[130:133], v[196:199], v[110:113]
	v_mfma_f32_16x16x32_bf16 v[106:109], v[142:145], v[196:199], v[106:109]
	v_mfma_f32_16x16x32_bf16 v[94:97], v[130:133], v[204:207], v[94:97]
	v_mfma_f32_16x16x32_bf16 v[90:93], v[142:145], v[204:207], v[90:93]
	v_mfma_f32_16x16x32_bf16 v[78:81], v[130:133], v[230:233], v[78:81]
	v_mfma_f32_16x16x32_bf16 v[74:77], v[142:145], v[230:233], v[74:77]
	s_setprio 0
	s_setprio 1
	v_mfma_f32_16x16x32_bf16 v[118:121], v[146:149], v[182:185], v[118:121]
	v_mfma_f32_16x16x32_bf16 v[114:117], v[154:157], v[182:185], v[114:117]
	v_mfma_f32_16x16x32_bf16 v[102:105], v[146:149], v[190:193], v[102:105]
	v_mfma_f32_16x16x32_bf16 v[98:101], v[154:157], v[190:193], v[98:101]
	v_mfma_f32_16x16x32_bf16 v[86:89], v[146:149], v[200:203], v[86:89]
	v_mfma_f32_16x16x32_bf16 v[82:85], v[154:157], v[200:203], v[82:85]
	v_mfma_f32_16x16x32_bf16 v[70:73], v[146:149], v[208:211], v[70:73]
	v_mfma_f32_16x16x32_bf16 v[66:69], v[154:157], v[208:211], v[66:69]
	v_mfma_f32_16x16x32_bf16 v[118:121], v[150:153], v[186:189], v[118:121]
	v_mfma_f32_16x16x32_bf16 v[114:117], v[158:161], v[186:189], v[114:117]
	v_mfma_f32_16x16x32_bf16 v[102:105], v[150:153], v[196:199], v[102:105]
	v_mfma_f32_16x16x32_bf16 v[98:101], v[158:161], v[196:199], v[98:101]
	v_mfma_f32_16x16x32_bf16 v[86:89], v[150:153], v[204:207], v[86:89]
	v_mfma_f32_16x16x32_bf16 v[82:85], v[158:161], v[204:207], v[82:85]
	v_mfma_f32_16x16x32_bf16 v[70:73], v[150:153], v[230:233], v[70:73]
	v_mfma_f32_16x16x32_bf16 v[66:69], v[158:161], v[230:233], v[66:69]
	s_setprio 0
	s_barrier
	s_add_i32 s28, s28, s43
	v_lshl_add_u64 v[234:235], s[12:13], 0, v[162:163]
	s_mov_b32 m0, s28
	ds_read_b128 v[182:185], v229 offset:16384
	ds_read_b128 v[186:189], v229 offset:17408
	ds_read_b128 v[190:193], v229 offset:18432
	ds_read_b128 v[196:199], v229 offset:19456
	ds_read_b128 v[200:203], v229 offset:20480
	ds_read_b128 v[204:207], v229 offset:21504
	ds_read_b128 v[208:211], v229 offset:22528
	ds_read_b128 v[230:233], v229 offset:23552
	global_load_lds_dwordx4 v[234:235], off
	s_add_i32 m0, s28, 0x2000
	s_add_u32 s28, s12, 0x80000
	v_lshl_add_u64 v[236:237], s[12:13], 0, v[164:165]
	s_addc_u32 s29, s13, 0
	s_add_i32 s33, s33, s43
	global_load_lds_dwordx4 v[236:237], off
	v_lshl_add_u64 v[238:239], s[28:29], 0, v[162:163]
	s_mov_b32 m0, s33
	v_lshl_add_u64 v[240:241], s[66:67], 0, v[168:169]
	global_load_lds_dwordx4 v[238:239], off
	v_lshl_add_u64 v[238:239], s[28:29], 0, v[164:165]
	s_add_i32 m0, s33, 0x2000
	s_nop 0
	global_load_lds_dwordx4 v[238:239], off
	v_lshl_add_u64 v[238:239], s[66:67], 0, v[166:167]
	s_mov_b32 m0, s59
	s_nop 0
	global_load_lds_dwordx4 v[238:239], off
	s_mov_b32 m0, s36
	s_nop 0
	global_load_lds_dwordx4 v[240:241], off
	s_waitcnt vmcnt(8)
	s_waitcnt lgkmcnt(0)
	s_barrier
; #define PG8_STAGE(bufoff, gbase, voff) do { _Pragma("unroll") for (int _i = 0; _i < 2; ++_i) \
;         __builtin_amdgcn_global_load_lds((const unsigned*)((const char*)(gbase) + (voff)[_i]), (LAS unsigned*)(lds + (bufoff) + ldsw + _i * 8192), 16, 0, 0); } while (0)
; #define PG8_LDA(dst, b, h) do { _Pragma("unroll") for (int m = 0; m < 4; ++m) _Pragma("unroll") for (int k = 0; k < 2; ++k) dst[m][k] = *(const LAS bf16x8*)(lds + PG8_SA(b, h) + aoff + m * 2048 + k * 1024); } while (0)
; #define PG8_LDB(dst, b, h) do { _Pragma("unroll") for (int n = 0; n < 2; ++n) _Pragma("unroll") for (int k = 0; k < 2; ++k) dst[n][k] = *(const LAS bf16x8*)(lds + PG8_SB(b, h) + boff + n * 2048 + k * 1024); } while (0)
; #define PG8_MMA(ai, bj, At, Bt) do { __builtin_amdgcn_s_setprio(1); _Pragma("unroll") for (int m = 0; m < 4; ++m) _Pragma("unroll") for (int n = 0; n < 2; ++n) _Pragma("unroll") for (int k = 0; k < 2; ++k) \
;         acc[ai][bj][m][n] = __builtin_amdgcn_mfma_f32_16x16x32_bf16(Bt[n][k], At[m][k], acc[ai][bj][m][n], 0, 0, 0); __builtin_amdgcn_s_setprio(0); } while (0)
; #define PG8_WAIT_V(n) asm volatile("s_waitcnt vmcnt(" #n ")" ::: "memory")
; #define PG8_WAIT_L(n) asm volatile("s_waitcnt lgkmcnt(" #n ")" ::: "memory")
; #define PG8_BAR __builtin_amdgcn_s_barrier()
; #define PG8_SCHED __builtin_amdgcn_sched_barrier(0)
; template <class Epi, class Sched, bool GATHER = false>
; __device__ __forceinline__ void gemm_phase(LAS unsigned char* lds, const int lda, const int ldb, const int K, const Sched& S, const Epi& E, const int* gidx = nullptr) {
;     ...
;             PG8_LDA(At, 0, 1); PG8_STAGE(PG8_SB(0, 0), b2, voffB); PG8_STAGE(PG8_SB(0, 1), b2 + hstepB, voffB); PG8_STAGE(PG8_SA(0, 0), a2, o2[0]);
;             PG8_WAIT_V(8); PG8_WAIT_L(0); PG8_BAR; PG8_MMA(1, 0, At, B0); PG8_MMA(1, 1, At, B1); PG8_BAR; PG8_SCHED;
;             PG8_LDB(B0, 1, 0); PG8_LDB(B1, 1, 1); PG8_SCHED; PG8_LDA(At, 1, 0); PG8_STAGE(PG8_SA(0, 1), a2, o2[1]);
;             PG8_WAIT_V(8); PG8_WAIT_L(0); PG8_BAR; PG8_MMA(0, 0, At, B0); PG8_MMA(0, 1, At, B1); PG8_BAR; PG8_SCHED;
	s_setprio 1
	v_mfma_f32_16x16x32_bf16 v[62:65], v[126:129], v[182:185], v[62:65]
	v_mfma_f32_16x16x32_bf16 v[58:61], v[138:141], v[182:185], v[58:61]
	v_mfma_f32_16x16x32_bf16 v[46:49], v[126:129], v[190:193], v[46:49]
	v_mfma_f32_16x16x32_bf16 v[42:45], v[138:141], v[190:193], v[42:45]
	v_mfma_f32_16x16x32_bf16 v[30:33], v[126:129], v[200:203], v[30:33]
	v_mfma_f32_16x16x32_bf16 v[26:29], v[138:141], v[200:203], v[26:29]
	v_mfma_f32_16x16x32_bf16 v[14:17], v[126:129], v[208:211], v[14:17]
	v_mfma_f32_16x16x32_bf16 v[10:13], v[138:141], v[208:211], v[10:13]
	v_mfma_f32_16x16x32_bf16 v[62:65], v[130:133], v[186:189], v[62:65]
	v_mfma_f32_16x16x32_bf16 v[58:61], v[142:145], v[186:189], v[58:61]
	v_mfma_f32_16x16x32_bf16 v[46:49], v[130:133], v[196:199], v[46:49]
	v_mfma_f32_16x16x32_bf16 v[42:45], v[142:145], v[196:199], v[42:45]
	v_mfma_f32_16x16x32_bf16 v[30:33], v[130:133], v[204:207], v[30:33]
	v_mfma_f32_16x16x32_bf16 v[26:29], v[142:145], v[204:207], v[26:29]
	v_mfma_f32_16x16x32_bf16 v[14:17], v[130:133], v[230:233], v[14:17]
	v_mfma_f32_16x16x32_bf16 v[10:13], v[142:145], v[230:233], v[10:13]
	s_setprio 0
	s_setprio 1
	v_mfma_f32_16x16x32_bf16 v[54:57], v[146:149], v[182:185], v[54:57]
	v_mfma_f32_16x16x32_bf16 v[50:53], v[154:157], v[182:185], v[50:53]
	v_mfma_f32_16x16x32_bf16 v[38:41], v[146:149], v[190:193], v[38:41]
	v_mfma_f32_16x16x32_bf16 v[34:37], v[154:157], v[190:193], v[34:37]
	v_mfma_f32_16x16x32_bf16 v[22:25], v[146:149], v[200:203], v[22:25]
	v_mfma_f32_16x16x32_bf16 v[18:21], v[154:157], v[200:203], v[18:21]
	v_mfma_f32_16x16x32_bf16 v[6:9], v[146:149], v[208:211], v[6:9]
	v_mfma_f32_16x16x32_bf16 v[2:5], v[154:157], v[208:211], v[2:5]
	v_mfma_f32_16x16x32_bf16 v[54:57], v[150:153], v[186:189], v[54:57]
	v_mfma_f32_16x16x32_bf16 v[50:53], v[158:161], v[186:189], v[50:53]
	v_mfma_f32_16x16x32_bf16 v[38:41], v[150:153], v[196:199], v[38:41]
	v_mfma_f32_16x16x32_bf16 v[34:37], v[158:161], v[196:199], v[34:37]
	v_mfma_f32_16x16x32_bf16 v[22:25], v[150:153], v[204:207], v[22:25]
	v_mfma_f32_16x16x32_bf16 v[18:21], v[158:161], v[204:207], v[18:21]
	v_mfma_f32_16x16x32_bf16 v[6:9], v[150:153], v[230:233], v[6:9]
	v_mfma_f32_16x16x32_bf16 v[2:5], v[158:161], v[230:233], v[2:5]
	s_setprio 0
	s_barrier
	s_add_i32 s28, 0, 0x18000
	s_add_i32 s29, 0, 0x1c000
	v_add_u32_e32 v142, s28, v175
	v_add_u32_e32 v158, s29, v175
	ds_read_b128 v[126:129], v142
	ds_read_b128 v[130:133], v142 offset:1024
	ds_read_b128 v[138:141], v142 offset:2048
	ds_read_b128 v[142:145], v142 offset:3072
	ds_read_b128 v[146:149], v158
	ds_read_b128 v[150:153], v158 offset:1024
	ds_read_b128 v[154:157], v158 offset:2048
	ds_read_b128 v[158:161], v158 offset:3072
	s_mov_b32 m0, s37
	v_lshl_add_u64 v[242:243], s[66:67], 0, v[170:171]
	ds_read_b128 v[182:185], v229 offset:32768
	ds_read_b128 v[186:189], v229 offset:33792
	ds_read_b128 v[190:193], v229 offset:34816
	ds_read_b128 v[196:199], v229 offset:35840
	ds_read_b128 v[200:203], v229 offset:36864
	ds_read_b128 v[204:207], v229 offset:37888
	ds_read_b128 v[208:211], v229 offset:38912
	ds_read_b128 v[230:233], v229 offset:39936
	global_load_lds_dwordx4 v[242:243], off
	v_lshl_add_u64 v[242:243], s[66:67], 0, v[172:173]
	s_mov_b32 m0, s22
	s_nop 0
	global_load_lds_dwordx4 v[242:243], off
	s_waitcnt vmcnt(8)
	s_waitcnt lgkmcnt(0)
	s_barrier
	s_setprio 1
	v_mfma_f32_16x16x32_bf16 v[134:137], v[126:129], v[182:185], v[134:137]
	v_mfma_f32_16x16x32_bf16 v[122:125], v[138:141], v[182:185], v[122:125]
	v_mfma_f32_16x16x32_bf16 v[110:113], v[126:129], v[190:193], v[110:113]
	v_mfma_f32_16x16x32_bf16 v[106:109], v[138:141], v[190:193], v[106:109]
	v_mfma_f32_16x16x32_bf16 v[94:97], v[126:129], v[200:203], v[94:97]
	v_mfma_f32_16x16x32_bf16 v[90:93], v[138:141], v[200:203], v[90:93]
	v_mfma_f32_16x16x32_bf16 v[78:81], v[126:129], v[208:211], v[78:81]
	v_mfma_f32_16x16x32_bf16 v[74:77], v[138:141], v[208:211], v[74:77]
	v_mfma_f32_16x16x32_bf16 v[134:137], v[130:133], v[186:189], v[134:137]
	v_mfma_f32_16x16x32_bf16 v[122:125], v[142:145], v[186:189], v[122:125]
	v_mfma_f32_16x16x32_bf16 v[110:113], v[130:133], v[196:199], v[110:113]
	v_mfma_f32_16x16x32_bf16 v[106:109], v[142:145], v[196:199], v[106:109]
	v_mfma_f32_16x16x32_bf16 v[94:97], v[130:133], v[204:207], v[94:97]
	v_mfma_f32_16x16x32_bf16 v[90:93], v[142:145], v[204:207], v[90:93]
	v_mfma_f32_16x16x32_bf16 v[78:81], v[130:133], v[230:233], v[78:81]
	v_mfma_f32_16x16x32_bf16 v[74:77], v[142:145], v[230:233], v[74:77]
	s_setprio 0
	s_setprio 1
	v_mfma_f32_16x16x32_bf16 v[118:121], v[146:149], v[182:185], v[118:121]
	v_mfma_f32_16x16x32_bf16 v[114:117], v[154:157], v[182:185], v[114:117]
	v_mfma_f32_16x16x32_bf16 v[102:105], v[146:149], v[190:193], v[102:105]
	v_mfma_f32_16x16x32_bf16 v[98:101], v[154:157], v[190:193], v[98:101]
	v_mfma_f32_16x16x32_bf16 v[86:89], v[146:149], v[200:203], v[86:89]
	v_mfma_f32_16x16x32_bf16 v[82:85], v[154:157], v[200:203], v[82:85]
	v_mfma_f32_16x16x32_bf16 v[70:73], v[146:149], v[208:211], v[70:73]
	v_mfma_f32_16x16x32_bf16 v[66:69], v[154:157], v[208:211], v[66:69]
	v_mfma_f32_16x16x32_bf16 v[118:121], v[150:153], v[186:189], v[118:121]
	v_mfma_f32_16x16x32_bf16 v[114:117], v[158:161], v[186:189], v[114:117]
	v_mfma_f32_16x16x32_bf16 v[102:105], v[150:153], v[196:199], v[102:105]
	v_mfma_f32_16x16x32_bf16 v[98:101], v[158:161], v[196:199], v[98:101]
	v_mfma_f32_16x16x32_bf16 v[86:89], v[150:153], v[204:207], v[86:89]
	v_mfma_f32_16x16x32_bf16 v[82:85], v[158:161], v[204:207], v[82:85]
	v_mfma_f32_16x16x32_bf16 v[70:73], v[150:153], v[230:233], v[70:73]
	v_mfma_f32_16x16x32_bf16 v[66:69], v[158:161], v[230:233], v[66:69]
	s_setprio 0
	s_barrier
; #define PG8_STAGE(bufoff, gbase, voff) do { _Pragma("unroll") for (int _i = 0; _i < 2; ++_i) \
;         __builtin_amdgcn_global_load_lds((const unsigned*)((const char*)(gbase) + (voff)[_i]), (LAS unsigned*)(lds + (bufoff) + ldsw + _i * 8192), 16, 0, 0); } while (0)
; #define PG8_LDA(dst, b, h) do { _Pragma("unroll") for (int m = 0; m < 4; ++m) _Pragma("unroll") for (int k = 0; k < 2; ++k) dst[m][k] = *(const LAS bf16x8*)(lds + PG8_SA(b, h) + aoff + m * 2048 + k * 1024); } while (0)
; #define PG8_LDB(dst, b, h) do { _Pragma("unroll") for (int n = 0; n < 2; ++n) _Pragma("unroll") for (int k = 0; k < 2; ++k) dst[n][k] = *(const LAS bf16x8*)(lds + PG8_SB(b, h) + boff + n * 2048 + k * 1024); } while (0)
; #define PG8_MMA(ai, bj, At, Bt) do { __builtin_amdgcn_s_setprio(1); _Pragma("unroll") for (int m = 0; m < 4; ++m) _Pragma("unroll") for (int n = 0; n < 2; ++n) _Pragma("unroll") for (int k = 0; k < 2; ++k) \
;         acc[ai][bj][m][n] = __builtin_amdgcn_mfma_f32_16x16x32_bf16(Bt[n][k], At[m][k], acc[ai][bj][m][n], 0, 0, 0); __builtin_amdgcn_s_setprio(0); } while (0)
; #define PG8_WAIT_V(n) asm volatile("s_waitcnt vmcnt(" #n ")" ::: "memory")
; #define PG8_WAIT_L(n) asm volatile("s_waitcnt lgkmcnt(" #n ")" ::: "memory")
; #define PG8_BAR __builtin_amdgcn_s_barrier()
; #define PG8_SCHED __builtin_amdgcn_sched_barrier(0)
; template <class Epi, class Sched, bool GATHER = false>
; __device__ __forceinline__ void gemm_phase(LAS unsigned char* lds, const int lda, const int ldb, const int K, const Sched& S, const Epi& E, const int* gidx = nullptr) {
;     ...
;             PG8_LDB(B0, 1, 0); PG8_LDB(B1, 1, 1); PG8_SCHED; PG8_LDA(At, 1, 0); PG8_STAGE(PG8_SA(0, 1), a2, o2[1]);
;             PG8_WAIT_V(8); PG8_WAIT_L(0); PG8_BAR; PG8_MMA(0, 0, At, B0); PG8_MMA(0, 1, At, B1); PG8_BAR; PG8_SCHED;
;             PG8_LDA(At, 1, 1); PG8_STAGE(PG8_SB(1, 0), b3, voffB); PG8_STAGE(PG8_SB(1, 1), b3 + hstepB, voffB); PG8_STAGE(PG8_SA(1, 0), a3, o2[0]);
;             PG8_WAIT_V(8); PG8_WAIT_L(0); PG8_BAR; PG8_MMA(1, 0, At, B0); PG8_MMA(1, 1, At, B1); PG8_BAR; PG8_SCHED;
;         }
	s_add_i32 s28, s28, s43
	v_lshl_add_u64 v[234:235], v[234:235], 0, s[64:65]
	s_mov_b32 m0, s28
	ds_read_b128 v[182:185], v229 offset:49152
	ds_read_b128 v[186:189], v229 offset:50176
	ds_read_b128 v[190:193], v229 offset:51200
	ds_read_b128 v[196:199], v229 offset:52224
	ds_read_b128 v[200:203], v229 offset:53248
	ds_read_b128 v[204:207], v229 offset:54272
	ds_read_b128 v[208:211], v229 offset:55296
	ds_read_b128 v[230:233], v229 offset:56320
	global_load_lds_dwordx4 v[234:235], off
	s_add_i32 m0, s28, 0x2000
	s_add_u32 s12, s12, 0x80080
	v_lshl_add_u64 v[234:235], v[236:237], 0, s[64:65]
	s_addc_u32 s13, s13, 0
	s_add_i32 s28, s29, s43
	global_load_lds_dwordx4 v[234:235], off
	v_lshl_add_u64 v[234:235], s[12:13], 0, v[162:163]
	s_mov_b32 m0, s28
	s_nop 0
	global_load_lds_dwordx4 v[234:235], off
	v_lshl_add_u64 v[234:235], s[12:13], 0, v[164:165]
	s_add_i32 m0, s28, 0x2000
	s_nop 0
	global_load_lds_dwordx4 v[234:235], off
	v_lshl_add_u64 v[234:235], v[238:239], 0, s[64:65]
	s_mov_b32 m0, s10
	s_nop 0
	global_load_lds_dwordx4 v[234:235], off
	v_lshl_add_u64 v[234:235], v[240:241], 0, s[64:65]
	s_mov_b32 m0, s11
	s_nop 0
	global_load_lds_dwordx4 v[234:235], off
	s_waitcnt vmcnt(8)
	s_waitcnt lgkmcnt(0)
	s_barrier
	s_setprio 1
	v_mfma_f32_16x16x32_bf16 v[62:65], v[126:129], v[182:185], v[62:65]
	v_mfma_f32_16x16x32_bf16 v[58:61], v[138:141], v[182:185], v[58:61]
	v_mfma_f32_16x16x32_bf16 v[46:49], v[126:129], v[190:193], v[46:49]
	v_mfma_f32_16x16x32_bf16 v[42:45], v[138:141], v[190:193], v[42:45]
	v_mfma_f32_16x16x32_bf16 v[30:33], v[126:129], v[200:203], v[30:33]
	v_mfma_f32_16x16x32_bf16 v[26:29], v[138:141], v[200:203], v[26:29]
	v_mfma_f32_16x16x32_bf16 v[14:17], v[126:129], v[208:211], v[14:17]
	v_mfma_f32_16x16x32_bf16 v[10:13], v[138:141], v[208:211], v[10:13]
	v_mfma_f32_16x16x32_bf16 v[62:65], v[130:133], v[186:189], v[62:65]
	v_mfma_f32_16x16x32_bf16 v[58:61], v[142:145], v[186:189], v[58:61]
	v_mfma_f32_16x16x32_bf16 v[46:49], v[130:133], v[196:199], v[46:49]
	v_mfma_f32_16x16x32_bf16 v[42:45], v[142:145], v[196:199], v[42:45]
	v_mfma_f32_16x16x32_bf16 v[30:33], v[130:133], v[204:207], v[30:33]
	v_mfma_f32_16x16x32_bf16 v[26:29], v[142:145], v[204:207], v[26:29]
	v_mfma_f32_16x16x32_bf16 v[14:17], v[130:133], v[230:233], v[14:17]
	v_mfma_f32_16x16x32_bf16 v[10:13], v[142:145], v[230:233], v[10:13]
	s_setprio 0
	s_setprio 1
	v_mfma_f32_16x16x32_bf16 v[54:57], v[146:149], v[182:185], v[54:57]
	v_mfma_f32_16x16x32_bf16 v[50:53], v[154:157], v[182:185], v[50:53]
	v_mfma_f32_16x16x32_bf16 v[38:41], v[146:149], v[190:193], v[38:41]
	v_mfma_f32_16x16x32_bf16 v[34:37], v[154:157], v[190:193], v[34:37]
	v_mfma_f32_16x16x32_bf16 v[22:25], v[146:149], v[200:203], v[22:25]
	v_mfma_f32_16x16x32_bf16 v[18:21], v[154:157], v[200:203], v[18:21]
	v_mfma_f32_16x16x32_bf16 v[6:9], v[146:149], v[208:211], v[6:9]
	v_mfma_f32_16x16x32_bf16 v[2:5], v[154:157], v[208:211], v[2:5]
	v_mfma_f32_16x16x32_bf16 v[54:57], v[150:153], v[186:189], v[54:57]
	v_mfma_f32_16x16x32_bf16 v[50:53], v[158:161], v[186:189], v[50:53]
	v_mfma_f32_16x16x32_bf16 v[38:41], v[150:153], v[196:199], v[38:41]
	v_mfma_f32_16x16x32_bf16 v[34:37], v[158:161], v[196:199], v[34:37]
	v_mfma_f32_16x16x32_bf16 v[22:25], v[150:153], v[204:207], v[22:25]
	v_mfma_f32_16x16x32_bf16 v[18:21], v[158:161], v[204:207], v[18:21]
	v_mfma_f32_16x16x32_bf16 v[6:9], v[150:153], v[230:233], v[6:9]
	v_mfma_f32_16x16x32_bf16 v[2:5], v[158:161], v[230:233], v[2:5]
	s_setprio 0
	s_barrier
	s_add_i32 s75, s75, 2
	s_add_u32 s72, s72, 0x100
	s_addc_u32 s73, s73, 0
	s_add_u32 s60, s60, 0x100
	s_addc_u32 s74, s74, 0
	s_cmp_gt_u32 s75, 29
	s_cbranch_scc0 .LBB0_428
	s_and_b64 vcc, exec, s[48:49]
	s_cbranch_vccz .LBB0_431
	s_barrier

; #define PW_SYNC do { asm volatile("s_waitcnt lgkmcnt(0)" ::: "memory"); __builtin_amdgcn_s_barrier(); asm volatile("" ::: "memory"); } while (0)
; __device__ __forceinline__ void ph_weights(const Params& p, LAS unsigned char* lds, const int p0, const int p1, const int wi, const int wn) {
;     ...
;     int pi = p0 + wi; bool hA, hB;
;     PW_LOAD(pi, dA0, dA1, a0, a1, hA);
;     PW_LOAD(pi + wn, dB0, dB1, b0, b1, hB);
;     while (hA) {
;         { PW_TOLDS(dA0, a0, a1); PW_SYNC; const TDesc s0 = dA0, s1 = dA1; PW_LOAD(pi + 2 * wn, dA0, dA1, a0, a1, hA); PW_STORE(s0, s1); PW_SYNC; }
;         if (!hB) break;
;         { PW_TOLDS(dB0, b0, b1); PW_SYNC; const TDesc s0 = dB0, s1 = dB1; PW_LOAD(pi + 3 * wn, dB0, dB1, b0, b1, hB); PW_STORE(s0, s1); PW_SYNC; }
;         pi += 2 * wn;
;     }
; __global__ void __launch_bounds__(512, 2) mk_fwd(Params p) {
;     ...
;             } else { if (bx - MIX_GW < 4) ph_rbias(p, 0, bx - MIX_GW); ph_weights(p, lds, 240, 6880, bx - MIX_GW, G - MIX_GW); }
.LBB0_779:
	v_readlane_b32 s0, v249, 28
	s_nop 3
	s_cmpk_lt_u32 s0, 0xa0
	s_cbranch_scc1 .Lcv_late
	s_mul_i32 s0, s0, 2
	s_add_u32 s0, s0, 4294967216
	s_movk_i32 s70, 190
	s_movk_i32 s73, 2
	s_movk_i32 s71, 0x16b0
	s_movk_i32 s82, 0
	s_mov_b32 s74, 0
	v_writelane_b32 v255, s29, 61
	s_branch .Lcv_common
.Lcv_late:
	v_readlane_b32 s0, v249, 28
	s_nop 3
	s_mul_i32 s0, s0, 1
	s_add_u32 s0, s0, 5680
	s_movk_i32 s70, 31
	s_movk_i32 s73, 1
	s_movk_i32 s71, 0x1920
	s_mov_b32 s82, 0
	s_mov_b32 s74, 0
	v_writelane_b32 v255, s29, 61
	s_branch .Lcv_common
.Lcv_idle:
	v_writelane_b32 v246, s14, 0
	v_writelane_b32 v246, s15, 1
	v_writelane_b32 v246, s20, 2
	v_writelane_b32 v246, s21, 3
	v_writelane_b32 v246, s29, 4
	v_writelane_b32 v246, s30, 5
	v_writelane_b32 v246, s31, 6
	v_writelane_b32 v246, s36, 7
	v_writelane_b32 v246, s37, 8
	v_writelane_b32 v246, s56, 9
	v_writelane_b32 v246, s57, 10
	v_writelane_b32 v246, s69, 11
	s_mov_b32 s74, 1
	s_mov_b32 s82, 0
	s_waitcnt vmcnt(0) lgkmcnt(0)
	s_barrier
	v_readlane_b32 s0, v249, 28
	s_nop 3
	s_mul_i32 s0, s0, 1
	s_add_u32 s0, s0, 6464
	s_movk_i32 s70, 31
	s_movk_i32 s73, 1
	s_movk_i32 s71, 0x1ae0
	s_branch .Lcv_common
.Lcv_tail:
	v_writelane_b32 v246, s14, 0
	v_writelane_b32 v246, s15, 1
	v_writelane_b32 v246, s20, 2
	v_writelane_b32 v246, s21, 3
	v_writelane_b32 v246, s29, 4
	v_writelane_b32 v246, s30, 5
	v_writelane_b32 v246, s31, 6
	v_writelane_b32 v246, s36, 7
	v_writelane_b32 v246, s37, 8
	v_writelane_b32 v246, s56, 9
	v_writelane_b32 v246, s57, 10
	v_writelane_b32 v246, s69, 11
	s_mov_b32 s74, 2
	s_mov_b32 s82, 0
	s_waitcnt vmcnt(0) lgkmcnt(0)
	s_barrier
	v_readlane_b32 s0, v249, 28
	s_nop 3
	s_mul_i32 s0, s0, 1
	s_add_u32 s0, s0, 6432
	s_movk_i32 s70, 127
	s_movk_i32 s73, 1
	s_movk_i32 s71, 0x1a20

; #define PG8_STAGE(bufoff, gbase, voff) do { _Pragma("unroll") for (int _i = 0; _i < 2; ++_i) \
;         __builtin_amdgcn_global_load_lds((const unsigned*)((const char*)(gbase) + (voff)[_i]), (LAS unsigned*)(lds + (bufoff) + ldsw + _i * 8192), 16, 0, 0); } while (0)
; #define PG8_LDA(dst, b, h) do { _Pragma("unroll") for (int m = 0; m < 4; ++m) _Pragma("unroll") for (int k = 0; k < 2; ++k) dst[m][k] = *(const LAS bf16x8*)(lds + PG8_SA(b, h) + aoff + m * 2048 + k * 1024); } while (0)
; #define PG8_LDB(dst, b, h) do { _Pragma("unroll") for (int n = 0; n < 2; ++n) _Pragma("unroll") for (int k = 0; k < 2; ++k) dst[n][k] = *(const LAS bf16x8*)(lds + PG8_SB(b, h) + boff + n * 2048 + k * 1024); } while (0)
; #define PG8_MMA(ai, bj, At, Bt) do { __builtin_amdgcn_s_setprio(1); _Pragma("unroll") for (int m = 0; m < 4; ++m) _Pragma("unroll") for (int n = 0; n < 2; ++n) _Pragma("unroll") for (int k = 0; k < 2; ++k) \
;         acc[ai][bj][m][n] = __builtin_amdgcn_mfma_f32_16x16x32_bf16(Bt[n][k], At[m][k], acc[ai][bj][m][n], 0, 0, 0); __builtin_amdgcn_s_setprio(0); } while (0)
; #define PG8_BAR __builtin_amdgcn_s_barrier()
; template <class Epi, class Sched, bool GATHER = false>
; __device__ __forceinline__ void gemm_phase(LAS unsigned char* lds, const int lda, const int ldb, const int K, const Sched& S, const Epi& E, const int* gidx = nullptr) {
;     ...
;             const char* a1 = cA + (size_t)(t + 1) * kstep;
;             const char* a2 = last ? nA : cA + (size_t)(t + 2) * kstep; const char* b2 = last ? nB : cB + (size_t)(t + 2) * kstep;
;             const char* a3 = a2 + kstep; const char* b3 = b2 + kstep;
;             unsigned o2[2][2];
; #pragma unroll
;             for (int hh = 0; hh < 2; ++hh)
; #pragma unroll
;                 for (int i = 0; i < 2; ++i) { if constexpr (GATHER) o2[hh][i] = last ? ofn[hh][i] : ofc[hh][i]; else o2[hh][i] = ofc[hh][i]; }
;             PG8_LDB(B0, 0, 0); PG8_LDB(B1, 0, 1); PG8_SCHED; PG8_LDA(At, 0, 0); PG8_STAGE(PG8_SA(1, 1), a1, ofc[1]);
;             PG8_WAIT_V(8); PG8_WAIT_L(0); PG8_BAR; PG8_MMA(0, 0, At, B0); PG8_MMA(0, 1, At, B1); PG8_BAR; PG8_SCHED;
;             PG8_LDA(At, 0, 1); PG8_STAGE(PG8_SB(0, 0), b2, voffB); PG8_STAGE(PG8_SB(0, 1), b2 + hstepB, voffB); PG8_STAGE(PG8_SA(0, 0), a2, o2[0]);
;             PG8_WAIT_V(8); PG8_WAIT_L(0); PG8_BAR; PG8_MMA(1, 0, At, B0); PG8_MMA(1, 1, At, B1); PG8_BAR; PG8_SCHED;
.LBB0_1107:
	s_add_i32 s28, 0, 0x10000
	s_add_i32 s33, 0, 0x14000
	v_add_u32_e32 v86, s28, v178
	v_add_u32_e32 v172, s33, v178
	ds_read_b128 v[70:73], v86
	ds_read_b128 v[78:81], v86 offset:1024
	ds_read_b128 v[82:85], v86 offset:2048
	ds_read_b128 v[86:89], v86 offset:3072
	ds_read_b128 v[146:149], v172
	ds_read_b128 v[150:153], v172 offset:1024
	ds_read_b128 v[168:171], v172 offset:2048
	ds_read_b128 v[172:175], v172 offset:3072
	v_lshl_add_u64 v[176:177], s[34:35], 0, v[166:167]
	s_add_i32 m0, s59, 0xc000
	ds_read_b128 v[182:185], v180
	ds_read_b128 v[186:189], v180 offset:1024
	ds_read_b128 v[190:193], v180 offset:2048
	ds_read_b128 v[196:199], v180 offset:3072
	ds_read_b128 v[200:203], v180 offset:4096
	ds_read_b128 v[204:207], v180 offset:5120
	ds_read_b128 v[208:211], v180 offset:6144
	ds_read_b128 v[228:231], v180 offset:7168
	s_add_u32 s12, s34, 0x80
	s_addc_u32 s13, s35, 0
	s_cmp_eq_u32 s83, 28
	s_cselect_b32 s67, s71, s13
	s_cselect_b32 s66, s70, s12
	s_cselect_b32 s13, s73, s82
	s_cselect_b32 s12, s72, s69
	global_load_lds_dwordx4 v[176:177], off
	v_lshl_add_u64 v[176:177], s[34:35], 0, v[164:165]
	s_add_i32 m0, s59, 0xe000
	s_nop 0
	global_load_lds_dwordx4 v[176:177], off
	s_waitcnt vmcnt(8)
	s_waitcnt lgkmcnt(0)
	s_barrier
	s_setprio 1
	v_mfma_f32_16x16x32_bf16 v[142:145], v[70:73], v[182:185], v[142:145]
	v_mfma_f32_16x16x32_bf16 v[138:141], v[82:85], v[182:185], v[138:141]
	v_mfma_f32_16x16x32_bf16 v[126:129], v[70:73], v[190:193], v[126:129]
	v_mfma_f32_16x16x32_bf16 v[122:125], v[82:85], v[190:193], v[122:125]
	v_mfma_f32_16x16x32_bf16 v[110:113], v[70:73], v[200:203], v[110:113]
	v_mfma_f32_16x16x32_bf16 v[106:109], v[82:85], v[200:203], v[106:109]
	v_mfma_f32_16x16x32_bf16 v[94:97], v[70:73], v[208:211], v[94:97]
	v_mfma_f32_16x16x32_bf16 v[90:93], v[82:85], v[208:211], v[90:93]
	v_mfma_f32_16x16x32_bf16 v[142:145], v[78:81], v[186:189], v[142:145]
	v_mfma_f32_16x16x32_bf16 v[138:141], v[86:89], v[186:189], v[138:141]
	v_mfma_f32_16x16x32_bf16 v[126:129], v[78:81], v[196:199], v[126:129]
	v_mfma_f32_16x16x32_bf16 v[122:125], v[86:89], v[196:199], v[122:125]
	v_mfma_f32_16x16x32_bf16 v[110:113], v[78:81], v[204:207], v[110:113]
	v_mfma_f32_16x16x32_bf16 v[106:109], v[86:89], v[204:207], v[106:109]
	v_mfma_f32_16x16x32_bf16 v[94:97], v[78:81], v[228:231], v[94:97]
	v_mfma_f32_16x16x32_bf16 v[90:93], v[86:89], v[228:231], v[90:93]
	s_setprio 0
	s_setprio 1
	v_mfma_f32_16x16x32_bf16 v[134:137], v[146:149], v[182:185], v[134:137]
	v_mfma_f32_16x16x32_bf16 v[130:133], v[168:171], v[182:185], v[130:133]
	v_mfma_f32_16x16x32_bf16 v[118:121], v[146:149], v[190:193], v[118:121]
	v_mfma_f32_16x16x32_bf16 v[114:117], v[168:171], v[190:193], v[114:117]
	v_mfma_f32_16x16x32_bf16 v[102:105], v[146:149], v[200:203], v[102:105]
	v_mfma_f32_16x16x32_bf16 v[98:101], v[168:171], v[200:203], v[98:101]
	v_mfma_f32_16x16x32_bf16 v[74:77], v[146:149], v[208:211], v[74:77]
	v_mfma_f32_16x16x32_bf16 v[66:69], v[168:171], v[208:211], v[66:69]
	v_mfma_f32_16x16x32_bf16 v[134:137], v[150:153], v[186:189], v[134:137]
	v_mfma_f32_16x16x32_bf16 v[130:133], v[172:175], v[186:189], v[130:133]
	v_mfma_f32_16x16x32_bf16 v[118:121], v[150:153], v[196:199], v[118:121]
	v_mfma_f32_16x16x32_bf16 v[114:117], v[172:175], v[196:199], v[114:117]
	v_mfma_f32_16x16x32_bf16 v[102:105], v[150:153], v[204:207], v[102:105]
	v_mfma_f32_16x16x32_bf16 v[98:101], v[172:175], v[204:207], v[98:101]
	v_mfma_f32_16x16x32_bf16 v[74:77], v[150:153], v[228:231], v[74:77]
	v_mfma_f32_16x16x32_bf16 v[66:69], v[172:175], v[228:231], v[66:69]
	s_setprio 0
	s_barrier
	s_add_i32 s28, s28, s8
	v_lshl_add_u64 v[176:177], s[12:13], 0, v[194:195]
	s_mov_b32 m0, s28
	ds_read_b128 v[182:185], v180 offset:16384
	ds_read_b128 v[186:189], v180 offset:17408
	ds_read_b128 v[190:193], v180 offset:18432
	ds_read_b128 v[196:199], v180 offset:19456
	ds_read_b128 v[200:203], v180 offset:20480
	ds_read_b128 v[204:207], v180 offset:21504
	ds_read_b128 v[208:211], v180 offset:22528
	ds_read_b128 v[228:231], v180 offset:23552
	global_load_lds_dwordx4 v[176:177], off
	s_add_i32 m0, s28, 0x2000
	s_add_u32 s28, s12, 0x80000
	v_lshl_add_u64 v[232:233], s[12:13], 0, v[154:155]
	s_addc_u32 s29, s13, 0
	s_add_i32 s33, s33, s8
	global_load_lds_dwordx4 v[232:233], off
	v_lshl_add_u64 v[234:235], s[28:29], 0, v[194:195]
	s_mov_b32 m0, s33
	v_lshl_add_u64 v[236:237], s[66:67], 0, v[158:159]
	global_load_lds_dwordx4 v[234:235], off
	v_lshl_add_u64 v[234:235], s[28:29], 0, v[154:155]
	s_add_i32 m0, s33, 0x2000
	s_nop 0
	global_load_lds_dwordx4 v[234:235], off
	v_lshl_add_u64 v[234:235], s[66:67], 0, v[156:157]
	s_mov_b32 m0, s59
	s_nop 0
	global_load_lds_dwordx4 v[234:235], off
	s_mov_b32 m0, s60
	s_nop 0
	global_load_lds_dwordx4 v[236:237], off
	s_waitcnt vmcnt(8)
	s_waitcnt lgkmcnt(0)
	s_barrier
; #define PG8_STAGE(bufoff, gbase, voff) do { _Pragma("unroll") for (int _i = 0; _i < 2; ++_i) \
;         __builtin_amdgcn_global_load_lds((const unsigned*)((const char*)(gbase) + (voff)[_i]), (LAS unsigned*)(lds + (bufoff) + ldsw + _i * 8192), 16, 0, 0); } while (0)
; #define PG8_LDA(dst, b, h) do { _Pragma("unroll") for (int m = 0; m < 4; ++m) _Pragma("unroll") for (int k = 0; k < 2; ++k) dst[m][k] = *(const LAS bf16x8*)(lds + PG8_SA(b, h) + aoff + m * 2048 + k * 1024); } while (0)
; #define PG8_LDB(dst, b, h) do { _Pragma("unroll") for (int n = 0; n < 2; ++n) _Pragma("unroll") for (int k = 0; k < 2; ++k) dst[n][k] = *(const LAS bf16x8*)(lds + PG8_SB(b, h) + boff + n * 2048 + k * 1024); } while (0)
; #define PG8_MMA(ai, bj, At, Bt) do { __builtin_amdgcn_s_setprio(1); _Pragma("unroll") for (int m = 0; m < 4; ++m) _Pragma("unroll") for (int n = 0; n < 2; ++n) _Pragma("unroll") for (int k = 0; k < 2; ++k) \
;         acc[ai][bj][m][n] = __builtin_amdgcn_mfma_f32_16x16x32_bf16(Bt[n][k], At[m][k], acc[ai][bj][m][n], 0, 0, 0); __builtin_amdgcn_s_setprio(0); } while (0)
; #define PG8_WAIT_V(n) asm volatile("s_waitcnt vmcnt(" #n ")" ::: "memory")
; #define PG8_WAIT_L(n) asm volatile("s_waitcnt lgkmcnt(" #n ")" ::: "memory")
; #define PG8_BAR __builtin_amdgcn_s_barrier()
; #define PG8_SCHED __builtin_amdgcn_sched_barrier(0)
; template <class Epi, class Sched, bool GATHER = false>
; __device__ __forceinline__ void gemm_phase(LAS unsigned char* lds, const int lda, const int ldb, const int K, const Sched& S, const Epi& E, const int* gidx = nullptr) {
;     ...
;             PG8_LDA(At, 0, 1); PG8_STAGE(PG8_SB(0, 0), b2, voffB); PG8_STAGE(PG8_SB(0, 1), b2 + hstepB, voffB); PG8_STAGE(PG8_SA(0, 0), a2, o2[0]);
;             PG8_WAIT_V(8); PG8_WAIT_L(0); PG8_BAR; PG8_MMA(1, 0, At, B0); PG8_MMA(1, 1, At, B1); PG8_BAR; PG8_SCHED;
;             PG8_LDB(B0, 1, 0); PG8_LDB(B1, 1, 1); PG8_SCHED; PG8_LDA(At, 1, 0); PG8_STAGE(PG8_SA(0, 1), a2, o2[1]);
;             PG8_WAIT_V(8); PG8_WAIT_L(0); PG8_BAR; PG8_MMA(0, 0, At, B0); PG8_MMA(0, 1, At, B1); PG8_BAR; PG8_SCHED;
	s_setprio 1
	v_mfma_f32_16x16x32_bf16 v[62:65], v[70:73], v[182:185], v[62:65]
	v_mfma_f32_16x16x32_bf16 v[58:61], v[82:85], v[182:185], v[58:61]
	v_mfma_f32_16x16x32_bf16 v[46:49], v[70:73], v[190:193], v[46:49]
	v_mfma_f32_16x16x32_bf16 v[38:41], v[82:85], v[190:193], v[38:41]
	v_mfma_f32_16x16x32_bf16 v[26:29], v[70:73], v[200:203], v[26:29]
	v_mfma_f32_16x16x32_bf16 v[18:21], v[82:85], v[200:203], v[18:21]
	v_mfma_f32_16x16x32_bf16 v[6:9], v[70:73], v[208:211], v[6:9]
	v_mfma_f32_16x16x32_bf16 v[2:5], v[82:85], v[208:211], v[2:5]
	v_mfma_f32_16x16x32_bf16 v[62:65], v[78:81], v[186:189], v[62:65]
	v_mfma_f32_16x16x32_bf16 v[58:61], v[86:89], v[186:189], v[58:61]
	v_mfma_f32_16x16x32_bf16 v[46:49], v[78:81], v[196:199], v[46:49]
	v_mfma_f32_16x16x32_bf16 v[38:41], v[86:89], v[196:199], v[38:41]
	v_mfma_f32_16x16x32_bf16 v[26:29], v[78:81], v[204:207], v[26:29]
	v_mfma_f32_16x16x32_bf16 v[18:21], v[86:89], v[204:207], v[18:21]
	v_mfma_f32_16x16x32_bf16 v[6:9], v[78:81], v[228:231], v[6:9]
	v_mfma_f32_16x16x32_bf16 v[2:5], v[86:89], v[228:231], v[2:5]
	s_setprio 0
	s_setprio 1
	v_mfma_f32_16x16x32_bf16 v[54:57], v[146:149], v[182:185], v[54:57]
	v_mfma_f32_16x16x32_bf16 v[50:53], v[168:171], v[182:185], v[50:53]
	v_mfma_f32_16x16x32_bf16 v[42:45], v[146:149], v[190:193], v[42:45]
	v_mfma_f32_16x16x32_bf16 v[34:37], v[168:171], v[190:193], v[34:37]
	v_mfma_f32_16x16x32_bf16 v[30:33], v[146:149], v[200:203], v[30:33]
	v_mfma_f32_16x16x32_bf16 v[22:25], v[168:171], v[200:203], v[22:25]
	v_mfma_f32_16x16x32_bf16 v[14:17], v[146:149], v[208:211], v[14:17]
	v_mfma_f32_16x16x32_bf16 v[10:13], v[168:171], v[208:211], v[10:13]
	v_mfma_f32_16x16x32_bf16 v[54:57], v[150:153], v[186:189], v[54:57]
	v_mfma_f32_16x16x32_bf16 v[50:53], v[172:175], v[186:189], v[50:53]
	v_mfma_f32_16x16x32_bf16 v[42:45], v[150:153], v[196:199], v[42:45]
	v_mfma_f32_16x16x32_bf16 v[34:37], v[172:175], v[196:199], v[34:37]
	v_mfma_f32_16x16x32_bf16 v[30:33], v[150:153], v[204:207], v[30:33]
	v_mfma_f32_16x16x32_bf16 v[22:25], v[172:175], v[204:207], v[22:25]
	v_mfma_f32_16x16x32_bf16 v[14:17], v[150:153], v[228:231], v[14:17]
	v_mfma_f32_16x16x32_bf16 v[10:13], v[172:175], v[228:231], v[10:13]
	s_setprio 0
	s_barrier
	s_add_i32 s28, 0, 0x18000
	s_add_i32 s29, 0, 0x1c000
	v_add_u32_e32 v86, s28, v178
	v_add_u32_e32 v172, s29, v178
	ds_read_b128 v[70:73], v86
	ds_read_b128 v[78:81], v86 offset:1024
	ds_read_b128 v[82:85], v86 offset:2048
	ds_read_b128 v[86:89], v86 offset:3072
	ds_read_b128 v[146:149], v172
	ds_read_b128 v[150:153], v172 offset:1024
	ds_read_b128 v[168:171], v172 offset:2048
	ds_read_b128 v[172:175], v172 offset:3072
	s_mov_b32 m0, s74
	v_lshl_add_u64 v[238:239], s[66:67], 0, v[160:161]
	ds_read_b128 v[182:185], v180 offset:32768
	ds_read_b128 v[186:189], v180 offset:33792
	ds_read_b128 v[190:193], v180 offset:34816
	ds_read_b128 v[196:199], v180 offset:35840
	ds_read_b128 v[200:203], v180 offset:36864
	ds_read_b128 v[204:207], v180 offset:37888
	ds_read_b128 v[208:211], v180 offset:38912
	ds_read_b128 v[228:231], v180 offset:39936
	global_load_lds_dwordx4 v[238:239], off
	v_lshl_add_u64 v[238:239], s[66:67], 0, v[162:163]
	s_mov_b32 m0, s75
	s_nop 0
	global_load_lds_dwordx4 v[238:239], off
	s_waitcnt vmcnt(8)
	s_waitcnt lgkmcnt(0)
	s_barrier
	s_setprio 1
	v_mfma_f32_16x16x32_bf16 v[142:145], v[70:73], v[182:185], v[142:145]
	v_mfma_f32_16x16x32_bf16 v[138:141], v[82:85], v[182:185], v[138:141]
	v_mfma_f32_16x16x32_bf16 v[126:129], v[70:73], v[190:193], v[126:129]
	v_mfma_f32_16x16x32_bf16 v[122:125], v[82:85], v[190:193], v[122:125]
	v_mfma_f32_16x16x32_bf16 v[110:113], v[70:73], v[200:203], v[110:113]
	v_mfma_f32_16x16x32_bf16 v[106:109], v[82:85], v[200:203], v[106:109]
	v_mfma_f32_16x16x32_bf16 v[94:97], v[70:73], v[208:211], v[94:97]
	v_mfma_f32_16x16x32_bf16 v[90:93], v[82:85], v[208:211], v[90:93]
	v_mfma_f32_16x16x32_bf16 v[142:145], v[78:81], v[186:189], v[142:145]
	v_mfma_f32_16x16x32_bf16 v[138:141], v[86:89], v[186:189], v[138:141]
	v_mfma_f32_16x16x32_bf16 v[126:129], v[78:81], v[196:199], v[126:129]
	v_mfma_f32_16x16x32_bf16 v[122:125], v[86:89], v[196:199], v[122:125]
	v_mfma_f32_16x16x32_bf16 v[110:113], v[78:81], v[204:207], v[110:113]
	v_mfma_f32_16x16x32_bf16 v[106:109], v[86:89], v[204:207], v[106:109]
	v_mfma_f32_16x16x32_bf16 v[94:97], v[78:81], v[228:231], v[94:97]
	v_mfma_f32_16x16x32_bf16 v[90:93], v[86:89], v[228:231], v[90:93]
	s_setprio 0
	s_setprio 1
	v_mfma_f32_16x16x32_bf16 v[134:137], v[146:149], v[182:185], v[134:137]
	v_mfma_f32_16x16x32_bf16 v[130:133], v[168:171], v[182:185], v[130:133]
	v_mfma_f32_16x16x32_bf16 v[118:121], v[146:149], v[190:193], v[118:121]
	v_mfma_f32_16x16x32_bf16 v[114:117], v[168:171], v[190:193], v[114:117]
	v_mfma_f32_16x16x32_bf16 v[102:105], v[146:149], v[200:203], v[102:105]
	v_mfma_f32_16x16x32_bf16 v[98:101], v[168:171], v[200:203], v[98:101]
	v_mfma_f32_16x16x32_bf16 v[74:77], v[146:149], v[208:211], v[74:77]
	v_mfma_f32_16x16x32_bf16 v[66:69], v[168:171], v[208:211], v[66:69]
	v_mfma_f32_16x16x32_bf16 v[134:137], v[150:153], v[186:189], v[134:137]
	v_mfma_f32_16x16x32_bf16 v[130:133], v[172:175], v[186:189], v[130:133]
	v_mfma_f32_16x16x32_bf16 v[118:121], v[150:153], v[196:199], v[118:121]
	v_mfma_f32_16x16x32_bf16 v[114:117], v[172:175], v[196:199], v[114:117]
	v_mfma_f32_16x16x32_bf16 v[102:105], v[150:153], v[204:207], v[102:105]
	v_mfma_f32_16x16x32_bf16 v[98:101], v[172:175], v[204:207], v[98:101]
	v_mfma_f32_16x16x32_bf16 v[74:77], v[150:153], v[228:231], v[74:77]
	v_mfma_f32_16x16x32_bf16 v[66:69], v[172:175], v[228:231], v[66:69]
	s_setprio 0
	s_barrier
; #define PG8_STAGE(bufoff, gbase, voff) do { _Pragma("unroll") for (int _i = 0; _i < 2; ++_i) \
;         __builtin_amdgcn_global_load_lds((const unsigned*)((const char*)(gbase) + (voff)[_i]), (LAS unsigned*)(lds + (bufoff) + ldsw + _i * 8192), 16, 0, 0); } while (0)
; #define PG8_LDA(dst, b, h) do { _Pragma("unroll") for (int m = 0; m < 4; ++m) _Pragma("unroll") for (int k = 0; k < 2; ++k) dst[m][k] = *(const LAS bf16x8*)(lds + PG8_SA(b, h) + aoff + m * 2048 + k * 1024); } while (0)
; #define PG8_LDB(dst, b, h) do { _Pragma("unroll") for (int n = 0; n < 2; ++n) _Pragma("unroll") for (int k = 0; k < 2; ++k) dst[n][k] = *(const LAS bf16x8*)(lds + PG8_SB(b, h) + boff + n * 2048 + k * 1024); } while (0)
; #define PG8_MMA(ai, bj, At, Bt) do { __builtin_amdgcn_s_setprio(1); _Pragma("unroll") for (int m = 0; m < 4; ++m) _Pragma("unroll") for (int n = 0; n < 2; ++n) _Pragma("unroll") for (int k = 0; k < 2; ++k) \
;         acc[ai][bj][m][n] = __builtin_amdgcn_mfma_f32_16x16x32_bf16(Bt[n][k], At[m][k], acc[ai][bj][m][n], 0, 0, 0); __builtin_amdgcn_s_setprio(0); } while (0)
; #define PG8_WAIT_V(n) asm volatile("s_waitcnt vmcnt(" #n ")" ::: "memory")
; #define PG8_WAIT_L(n) asm volatile("s_waitcnt lgkmcnt(" #n ")" ::: "memory")
; #define PG8_BAR __builtin_amdgcn_s_barrier()
; #define PG8_SCHED __builtin_amdgcn_sched_barrier(0)
; template <class Epi, class Sched, bool GATHER = false>
; __device__ __forceinline__ void gemm_phase(LAS unsigned char* lds, const int lda, const int ldb, const int K, const Sched& S, const Epi& E, const int* gidx = nullptr) {
;     ...
;             PG8_LDB(B0, 1, 0); PG8_LDB(B1, 1, 1); PG8_SCHED; PG8_LDA(At, 1, 0); PG8_STAGE(PG8_SA(0, 1), a2, o2[1]);
;             PG8_WAIT_V(8); PG8_WAIT_L(0); PG8_BAR; PG8_MMA(0, 0, At, B0); PG8_MMA(0, 1, At, B1); PG8_BAR; PG8_SCHED;
;             PG8_LDA(At, 1, 1); PG8_STAGE(PG8_SB(1, 0), b3, voffB); PG8_STAGE(PG8_SB(1, 1), b3 + hstepB, voffB); PG8_STAGE(PG8_SA(1, 0), a3, o2[0]);
;             PG8_WAIT_V(8); PG8_WAIT_L(0); PG8_BAR; PG8_MMA(1, 0, At, B0); PG8_MMA(1, 1, At, B1); PG8_BAR; PG8_SCHED;
;         }
	s_add_i32 s28, s28, s8
	v_lshl_add_u64 v[176:177], v[176:177], 0, s[64:65]
	s_mov_b32 m0, s28
	ds_read_b128 v[182:185], v180 offset:49152
	ds_read_b128 v[186:189], v180 offset:50176
	ds_read_b128 v[190:193], v180 offset:51200
	ds_read_b128 v[196:199], v180 offset:52224
	ds_read_b128 v[200:203], v180 offset:53248
	ds_read_b128 v[204:207], v180 offset:54272
	ds_read_b128 v[208:211], v180 offset:55296
	ds_read_b128 v[228:231], v180 offset:56320
	global_load_lds_dwordx4 v[176:177], off
	s_add_i32 m0, s28, 0x2000
	s_add_u32 s12, s12, 0x80080
	v_lshl_add_u64 v[176:177], v[232:233], 0, s[64:65]
	s_addc_u32 s13, s13, 0
	s_add_i32 s28, s29, s8
	global_load_lds_dwordx4 v[176:177], off
	v_lshl_add_u64 v[176:177], s[12:13], 0, v[194:195]
	s_mov_b32 m0, s28
	s_nop 0
	global_load_lds_dwordx4 v[176:177], off
	v_lshl_add_u64 v[176:177], s[12:13], 0, v[154:155]
	s_add_i32 m0, s28, 0x2000
	s_nop 0
	global_load_lds_dwordx4 v[176:177], off
	v_lshl_add_u64 v[176:177], v[234:235], 0, s[64:65]
	s_mov_b32 m0, s76
	s_nop 0
	global_load_lds_dwordx4 v[176:177], off
	v_lshl_add_u64 v[176:177], v[236:237], 0, s[64:65]
	s_mov_b32 m0, s77
	s_nop 0
	global_load_lds_dwordx4 v[176:177], off
	s_waitcnt vmcnt(8)
	s_waitcnt lgkmcnt(0)
	s_barrier
	s_setprio 1
	v_mfma_f32_16x16x32_bf16 v[62:65], v[70:73], v[182:185], v[62:65]
	v_mfma_f32_16x16x32_bf16 v[58:61], v[82:85], v[182:185], v[58:61]
	v_mfma_f32_16x16x32_bf16 v[46:49], v[70:73], v[190:193], v[46:49]
	v_mfma_f32_16x16x32_bf16 v[38:41], v[82:85], v[190:193], v[38:41]
	v_mfma_f32_16x16x32_bf16 v[26:29], v[70:73], v[200:203], v[26:29]
	v_mfma_f32_16x16x32_bf16 v[18:21], v[82:85], v[200:203], v[18:21]
	v_mfma_f32_16x16x32_bf16 v[6:9], v[70:73], v[208:211], v[6:9]
	v_mfma_f32_16x16x32_bf16 v[2:5], v[82:85], v[208:211], v[2:5]
	v_mfma_f32_16x16x32_bf16 v[62:65], v[78:81], v[186:189], v[62:65]
	v_mfma_f32_16x16x32_bf16 v[58:61], v[86:89], v[186:189], v[58:61]
	v_mfma_f32_16x16x32_bf16 v[46:49], v[78:81], v[196:199], v[46:49]
	v_mfma_f32_16x16x32_bf16 v[38:41], v[86:89], v[196:199], v[38:41]
	v_mfma_f32_16x16x32_bf16 v[26:29], v[78:81], v[204:207], v[26:29]
	v_mfma_f32_16x16x32_bf16 v[18:21], v[86:89], v[204:207], v[18:21]
	v_mfma_f32_16x16x32_bf16 v[6:9], v[78:81], v[228:231], v[6:9]
	v_mfma_f32_16x16x32_bf16 v[2:5], v[86:89], v[228:231], v[2:5]
	s_setprio 0
	s_setprio 1
	v_mfma_f32_16x16x32_bf16 v[54:57], v[146:149], v[182:185], v[54:57]
	v_mfma_f32_16x16x32_bf16 v[50:53], v[168:171], v[182:185], v[50:53]
	v_mfma_f32_16x16x32_bf16 v[42:45], v[146:149], v[190:193], v[42:45]
	v_mfma_f32_16x16x32_bf16 v[34:37], v[168:171], v[190:193], v[34:37]
	v_mfma_f32_16x16x32_bf16 v[30:33], v[146:149], v[200:203], v[30:33]
	v_mfma_f32_16x16x32_bf16 v[22:25], v[168:171], v[200:203], v[22:25]
	v_mfma_f32_16x16x32_bf16 v[14:17], v[146:149], v[208:211], v[14:17]
	v_mfma_f32_16x16x32_bf16 v[10:13], v[168:171], v[208:211], v[10:13]
	v_mfma_f32_16x16x32_bf16 v[54:57], v[150:153], v[186:189], v[54:57]
	v_mfma_f32_16x16x32_bf16 v[50:53], v[172:175], v[186:189], v[50:53]
	v_mfma_f32_16x16x32_bf16 v[42:45], v[150:153], v[196:199], v[42:45]
	v_mfma_f32_16x16x32_bf16 v[34:37], v[172:175], v[196:199], v[34:37]
	v_mfma_f32_16x16x32_bf16 v[30:33], v[150:153], v[204:207], v[30:33]
	v_mfma_f32_16x16x32_bf16 v[22:25], v[172:175], v[204:207], v[22:25]
	v_mfma_f32_16x16x32_bf16 v[14:17], v[150:153], v[228:231], v[14:17]
	v_mfma_f32_16x16x32_bf16 v[10:13], v[172:175], v[228:231], v[10:13]
	s_setprio 0
	s_barrier
	s_add_i32 s83, s83, 2
	s_add_u32 s34, s34, 0x100
	s_addc_u32 s35, s35, 0
	s_add_u32 s69, s69, 0x100
	s_addc_u32 s82, s82, 0
	s_cmp_gt_u32 s83, 29
	s_cbranch_scc0 .LBB0_1107
	s_and_b64 vcc, exec, s[48:49]
	s_cbranch_vccz .LBB0_1110
	s_barrier

; #define PG8_STAGE(bufoff, gbase, voff) do { _Pragma("unroll") for (int _i = 0; _i < 2; ++_i) \
;         __builtin_amdgcn_global_load_lds((const unsigned*)((const char*)(gbase) + (voff)[_i]), (LAS unsigned*)(lds + (bufoff) + ldsw + _i * 8192), 16, 0, 0); } while (0)
; #define PG8_LDA(dst, b, h) do { _Pragma("unroll") for (int m = 0; m < 4; ++m) _Pragma("unroll") for (int k = 0; k < 2; ++k) dst[m][k] = *(const LAS bf16x8*)(lds + PG8_SA(b, h) + aoff + m * 2048 + k * 1024); } while (0)
; #define PG8_LDB(dst, b, h) do { _Pragma("unroll") for (int n = 0; n < 2; ++n) _Pragma("unroll") for (int k = 0; k < 2; ++k) dst[n][k] = *(const LAS bf16x8*)(lds + PG8_SB(b, h) + boff + n * 2048 + k * 1024); } while (0)
; #define PG8_MMA(ai, bj, At, Bt) do { __builtin_amdgcn_s_setprio(1); _Pragma("unroll") for (int m = 0; m < 4; ++m) _Pragma("unroll") for (int n = 0; n < 2; ++n) _Pragma("unroll") for (int k = 0; k < 2; ++k) \
;         acc[ai][bj][m][n] = __builtin_amdgcn_mfma_f32_16x16x32_bf16(Bt[n][k], At[m][k], acc[ai][bj][m][n], 0, 0, 0); __builtin_amdgcn_s_setprio(0); } while (0)
; #define PG8_BAR __builtin_amdgcn_s_barrier()
; template <class Epi, class Sched, bool GATHER = false>
; __device__ __forceinline__ void gemm_phase(LAS unsigned char* lds, const int lda, const int ldb, const int K, const Sched& S, const Epi& E, const int* gidx = nullptr) {
;     ...
;             const char* a1 = cA + (size_t)(t + 1) * kstep;
;             const char* a2 = last ? nA : cA + (size_t)(t + 2) * kstep; const char* b2 = last ? nB : cB + (size_t)(t + 2) * kstep;
;             const char* a3 = a2 + kstep; const char* b3 = b2 + kstep;
;             unsigned o2[2][2];
; #pragma unroll
;             for (int hh = 0; hh < 2; ++hh)
; #pragma unroll
;                 for (int i = 0; i < 2; ++i) { if constexpr (GATHER) o2[hh][i] = last ? ofn[hh][i] : ofc[hh][i]; else o2[hh][i] = ofc[hh][i]; }
;             PG8_LDB(B0, 0, 0); PG8_LDB(B1, 0, 1); PG8_SCHED; PG8_LDA(At, 0, 0); PG8_STAGE(PG8_SA(1, 1), a1, ofc[1]);
;             PG8_WAIT_V(8); PG8_WAIT_L(0); PG8_BAR; PG8_MMA(0, 0, At, B0); PG8_MMA(0, 1, At, B1); PG8_BAR; PG8_SCHED;
;             PG8_LDA(At, 0, 1); PG8_STAGE(PG8_SB(0, 0), b2, voffB); PG8_STAGE(PG8_SB(0, 1), b2 + hstepB, voffB); PG8_STAGE(PG8_SA(0, 0), a2, o2[0]);
;             PG8_WAIT_V(8); PG8_WAIT_L(0); PG8_BAR; PG8_MMA(1, 0, At, B0); PG8_MMA(1, 1, At, B1); PG8_BAR; PG8_SCHED;
.LBB0_1186:
	s_add_i32 s28, 0, 0x10000
	s_add_i32 s33, 0, 0x14000
	v_add_u32_e32 v102, s28, v84
	v_add_u32_e32 v118, s33, v84
	ds_read_b128 v[90:93], v102
	ds_read_b128 v[94:97], v102 offset:1024
	ds_read_b128 v[98:101], v102 offset:2048
	ds_read_b128 v[102:105], v102 offset:3072
	ds_read_b128 v[106:109], v118
	ds_read_b128 v[110:113], v118 offset:1024
	ds_read_b128 v[114:117], v118 offset:2048
	ds_read_b128 v[118:121], v118 offset:3072
	v_lshl_add_u64 v[204:205], v[82:83], 0, s[12:13]
	s_add_i32 m0, s51, 0xc000
	ds_read_b128 v[130:133], v85
	ds_read_b128 v[134:137], v85 offset:1024
	ds_read_b128 v[186:189], v85 offset:2048
	ds_read_b128 v[190:193], v85 offset:3072
	ds_read_b128 v[196:199], v85 offset:4096
	ds_read_b128 v[200:203], v85 offset:5120
	ds_read_b128 v[208:211], v85 offset:6144
	ds_read_b128 v[228:231], v85 offset:7168
	s_add_u32 s28, s74, s12
	s_addc_u32 s29, s75, s13
	s_add_u32 s28, s28, 0x100
	s_addc_u32 s29, s29, 0
	s_add_u32 s33, s68, s12
	s_addc_u32 s34, s69, s13
	s_cmpk_eq_i32 s12, 0xf00
	s_cselect_b32 s49, s75, s29
	s_cselect_b32 s48, s74, s28
	s_cselect_b32 s35, s45, s34
	s_cselect_b32 s34, s44, s33
	s_add_i32 s28, 0, 0x10000
	s_add_i32 s33, 0, 0x14000
	global_load_lds_dwordx4 v[204:205], off
	v_lshl_add_u64 v[204:205], v[80:81], 0, s[12:13]
	s_add_i32 m0, s51, 0xe000
	s_nop 0
	global_load_lds_dwordx4 v[204:205], off
	s_waitcnt vmcnt(8)
	s_waitcnt lgkmcnt(0)
	s_barrier
	s_setprio 1
	v_mfma_f32_16x16x32_bf16 v[182:185], v[90:93], v[130:133], v[182:185]
	v_mfma_f32_16x16x32_bf16 v[178:181], v[98:101], v[130:133], v[178:181]
	v_mfma_f32_16x16x32_bf16 v[166:169], v[90:93], v[186:189], v[166:169]
	v_mfma_f32_16x16x32_bf16 v[162:165], v[98:101], v[186:189], v[162:165]
	v_mfma_f32_16x16x32_bf16 v[150:153], v[90:93], v[196:199], v[150:153]
	v_mfma_f32_16x16x32_bf16 v[146:149], v[98:101], v[196:199], v[146:149]
	v_mfma_f32_16x16x32_bf16 v[126:129], v[90:93], v[208:211], v[126:129]
	v_mfma_f32_16x16x32_bf16 v[122:125], v[98:101], v[208:211], v[122:125]
	v_mfma_f32_16x16x32_bf16 v[182:185], v[94:97], v[134:137], v[182:185]
	v_mfma_f32_16x16x32_bf16 v[178:181], v[102:105], v[134:137], v[178:181]
	v_mfma_f32_16x16x32_bf16 v[166:169], v[94:97], v[190:193], v[166:169]
	v_mfma_f32_16x16x32_bf16 v[162:165], v[102:105], v[190:193], v[162:165]
	v_mfma_f32_16x16x32_bf16 v[150:153], v[94:97], v[200:203], v[150:153]
	v_mfma_f32_16x16x32_bf16 v[146:149], v[102:105], v[200:203], v[146:149]
	v_mfma_f32_16x16x32_bf16 v[126:129], v[94:97], v[228:231], v[126:129]
	v_mfma_f32_16x16x32_bf16 v[122:125], v[102:105], v[228:231], v[122:125]
	s_setprio 0
	s_setprio 1
	v_mfma_f32_16x16x32_bf16 v[174:177], v[106:109], v[130:133], v[174:177]
	v_mfma_f32_16x16x32_bf16 v[130:133], v[114:117], v[130:133], v[170:173]
	v_mfma_f32_16x16x32_bf16 v[154:157], v[114:117], v[186:189], v[154:157]
	v_mfma_f32_16x16x32_bf16 v[142:145], v[106:109], v[196:199], v[142:145]
	v_mfma_f32_16x16x32_bf16 v[138:141], v[114:117], v[196:199], v[138:141]
	v_mfma_f32_16x16x32_bf16 v[86:89], v[106:109], v[208:211], v[86:89]
	v_mfma_f32_16x16x32_bf16 v[74:77], v[114:117], v[208:211], v[74:77]
	v_mfma_f32_16x16x32_bf16 v[174:177], v[110:113], v[134:137], v[174:177]
	v_mfma_f32_16x16x32_bf16 v[130:133], v[118:121], v[134:137], v[130:133]
	v_mfma_f32_16x16x32_bf16 v[134:137], v[106:109], v[186:189], v[158:161]
	v_mfma_f32_16x16x32_bf16 v[154:157], v[118:121], v[190:193], v[154:157]
	v_mfma_f32_16x16x32_bf16 v[142:145], v[110:113], v[200:203], v[142:145]
	v_mfma_f32_16x16x32_bf16 v[138:141], v[118:121], v[200:203], v[138:141]
	v_mfma_f32_16x16x32_bf16 v[86:89], v[110:113], v[228:231], v[86:89]
	v_mfma_f32_16x16x32_bf16 v[74:77], v[118:121], v[228:231], v[74:77]
	v_mfma_f32_16x16x32_bf16 v[134:137], v[110:113], v[190:193], v[134:137]
	s_setprio 0
	s_barrier
	s_add_i32 s28, s28, s50
	v_lshl_add_u64 v[204:205], s[34:35], 0, v[194:195]
	s_mov_b32 m0, s28
	ds_read_b128 v[158:161], v85 offset:16384
	ds_read_b128 v[170:173], v85 offset:17408
	ds_read_b128 v[186:189], v85 offset:18432
	ds_read_b128 v[190:193], v85 offset:19456
	ds_read_b128 v[196:199], v85 offset:20480
	ds_read_b128 v[200:203], v85 offset:21504
	ds_read_b128 v[208:211], v85 offset:22528
	ds_read_b128 v[228:231], v85 offset:23552
	global_load_lds_dwordx4 v[204:205], off
	s_add_i32 m0, s28, 0x2000
	s_add_u32 s28, s34, 0x80000
	v_lshl_add_u64 v[232:233], s[34:35], 0, v[2:3]
	s_addc_u32 s29, s35, 0
	s_add_i32 s33, s33, s50
	global_load_lds_dwordx4 v[232:233], off
	v_lshl_add_u64 v[234:235], s[28:29], 0, v[194:195]
	s_mov_b32 m0, s33
	v_lshl_add_u64 v[236:237], s[48:49], 0, v[6:7]
	global_load_lds_dwordx4 v[234:235], off
	v_lshl_add_u64 v[234:235], s[28:29], 0, v[2:3]
	s_add_i32 m0, s33, 0x2000
	s_nop 0
	global_load_lds_dwordx4 v[234:235], off
	v_lshl_add_u64 v[234:235], s[48:49], 0, v[4:5]
	s_mov_b32 m0, s51
	s_nop 0
	global_load_lds_dwordx4 v[234:235], off
	s_mov_b32 m0, s60
	s_nop 0
	global_load_lds_dwordx4 v[236:237], off
	s_waitcnt vmcnt(8)
	s_waitcnt lgkmcnt(0)
	s_barrier
; #define PG8_STAGE(bufoff, gbase, voff) do { _Pragma("unroll") for (int _i = 0; _i < 2; ++_i) \
;         __builtin_amdgcn_global_load_lds((const unsigned*)((const char*)(gbase) + (voff)[_i]), (LAS unsigned*)(lds + (bufoff) + ldsw + _i * 8192), 16, 0, 0); } while (0)
; #define PG8_LDA(dst, b, h) do { _Pragma("unroll") for (int m = 0; m < 4; ++m) _Pragma("unroll") for (int k = 0; k < 2; ++k) dst[m][k] = *(const LAS bf16x8*)(lds + PG8_SA(b, h) + aoff + m * 2048 + k * 1024); } while (0)
; #define PG8_LDB(dst, b, h) do { _Pragma("unroll") for (int n = 0; n < 2; ++n) _Pragma("unroll") for (int k = 0; k < 2; ++k) dst[n][k] = *(const LAS bf16x8*)(lds + PG8_SB(b, h) + boff + n * 2048 + k * 1024); } while (0)
; #define PG8_MMA(ai, bj, At, Bt) do { __builtin_amdgcn_s_setprio(1); _Pragma("unroll") for (int m = 0; m < 4; ++m) _Pragma("unroll") for (int n = 0; n < 2; ++n) _Pragma("unroll") for (int k = 0; k < 2; ++k) \
;         acc[ai][bj][m][n] = __builtin_amdgcn_mfma_f32_16x16x32_bf16(Bt[n][k], At[m][k], acc[ai][bj][m][n], 0, 0, 0); __builtin_amdgcn_s_setprio(0); } while (0)
; #define PG8_BAR __builtin_amdgcn_s_barrier()
; template <class Epi, class Sched, bool GATHER = false>
; __device__ __forceinline__ void gemm_phase(LAS unsigned char* lds, const int lda, const int ldb, const int K, const Sched& S, const Epi& E, const int* gidx = nullptr) {
;     ...
;             PG8_LDB(B0, 0, 0); PG8_LDB(B1, 0, 1); PG8_SCHED; PG8_LDA(At, 0, 0); PG8_STAGE(PG8_SA(1, 1), a1, ofc[1]);
;             PG8_WAIT_V(8); PG8_WAIT_L(0); PG8_BAR; PG8_MMA(0, 0, At, B0); PG8_MMA(0, 1, At, B1); PG8_BAR; PG8_SCHED;
;             PG8_LDA(At, 0, 1); PG8_STAGE(PG8_SB(0, 0), b2, voffB); PG8_STAGE(PG8_SB(0, 1), b2 + hstepB, voffB); PG8_STAGE(PG8_SA(0, 0), a2, o2[0]);
;             PG8_WAIT_V(8); PG8_WAIT_L(0); PG8_BAR; PG8_MMA(1, 0, At, B0); PG8_MMA(1, 1, At, B1); PG8_BAR; PG8_SCHED;
;             PG8_LDB(B0, 1, 0); PG8_LDB(B1, 1, 1); PG8_SCHED; PG8_LDA(At, 1, 0); PG8_STAGE(PG8_SA(0, 1), a2, o2[1]);
;             PG8_WAIT_V(8); PG8_WAIT_L(0); PG8_BAR; PG8_MMA(0, 0, At, B0); PG8_MMA(0, 1, At, B1); PG8_BAR; PG8_SCHED;
;             PG8_LDA(At, 1, 1); PG8_STAGE(PG8_SB(1, 0), b3, voffB); PG8_STAGE(PG8_SB(1, 1), b3 + hstepB, voffB); PG8_STAGE(PG8_SA(1, 0), a3, o2[0]);
;             PG8_WAIT_V(8); PG8_WAIT_L(0); PG8_BAR; PG8_MMA(1, 0, At, B0); PG8_MMA(1, 1, At, B1); PG8_BAR; PG8_SCHED;
	s_setprio 1
	v_mfma_f32_16x16x32_bf16 v[70:73], v[90:93], v[158:161], v[70:73]
	v_mfma_f32_16x16x32_bf16 v[66:69], v[98:101], v[158:161], v[66:69]
	v_mfma_f32_16x16x32_bf16 v[54:57], v[90:93], v[186:189], v[54:57]
	v_mfma_f32_16x16x32_bf16 v[46:49], v[98:101], v[186:189], v[46:49]
	v_mfma_f32_16x16x32_bf16 v[34:37], v[90:93], v[196:199], v[34:37]
	v_mfma_f32_16x16x32_bf16 v[26:29], v[98:101], v[196:199], v[26:29]
	v_mfma_f32_16x16x32_bf16 v[22:25], v[90:93], v[208:211], v[22:25]
	v_mfma_f32_16x16x32_bf16 v[18:21], v[98:101], v[208:211], v[18:21]
	v_mfma_f32_16x16x32_bf16 v[70:73], v[94:97], v[170:173], v[70:73]
	v_mfma_f32_16x16x32_bf16 v[66:69], v[102:105], v[170:173], v[66:69]
	v_mfma_f32_16x16x32_bf16 v[54:57], v[94:97], v[190:193], v[54:57]
	v_mfma_f32_16x16x32_bf16 v[46:49], v[102:105], v[190:193], v[46:49]
	v_mfma_f32_16x16x32_bf16 v[34:37], v[94:97], v[200:203], v[34:37]
	v_mfma_f32_16x16x32_bf16 v[26:29], v[102:105], v[200:203], v[26:29]
	v_mfma_f32_16x16x32_bf16 v[22:25], v[94:97], v[228:231], v[22:25]
	v_mfma_f32_16x16x32_bf16 v[18:21], v[102:105], v[228:231], v[18:21]
	s_setprio 0
	s_setprio 1
	v_mfma_f32_16x16x32_bf16 v[62:65], v[106:109], v[158:161], v[62:65]
	v_mfma_f32_16x16x32_bf16 v[58:61], v[114:117], v[158:161], v[58:61]
	v_mfma_f32_16x16x32_bf16 v[50:53], v[106:109], v[186:189], v[50:53]
	v_mfma_f32_16x16x32_bf16 v[42:45], v[114:117], v[186:189], v[42:45]
	v_mfma_f32_16x16x32_bf16 v[38:41], v[106:109], v[196:199], v[38:41]
	v_mfma_f32_16x16x32_bf16 v[30:33], v[114:117], v[196:199], v[30:33]
	v_mfma_f32_16x16x32_bf16 v[14:17], v[106:109], v[208:211], v[14:17]
	v_mfma_f32_16x16x32_bf16 v[10:13], v[114:117], v[208:211], v[10:13]
	v_mfma_f32_16x16x32_bf16 v[62:65], v[110:113], v[170:173], v[62:65]
	v_mfma_f32_16x16x32_bf16 v[58:61], v[118:121], v[170:173], v[58:61]
	v_mfma_f32_16x16x32_bf16 v[50:53], v[110:113], v[190:193], v[50:53]
	v_mfma_f32_16x16x32_bf16 v[42:45], v[118:121], v[190:193], v[42:45]
	v_mfma_f32_16x16x32_bf16 v[38:41], v[110:113], v[200:203], v[38:41]
	v_mfma_f32_16x16x32_bf16 v[30:33], v[118:121], v[200:203], v[30:33]
	v_mfma_f32_16x16x32_bf16 v[14:17], v[110:113], v[228:231], v[14:17]
	v_mfma_f32_16x16x32_bf16 v[10:13], v[118:121], v[228:231], v[10:13]
	s_setprio 0
	s_barrier
	s_add_i32 s28, 0, 0x18000
	s_add_i32 s33, 0, 0x1c000
	v_add_u32_e32 v102, s28, v84
	v_add_u32_e32 v118, s33, v84
	ds_read_b128 v[90:93], v102
	ds_read_b128 v[94:97], v102 offset:1024
	ds_read_b128 v[98:101], v102 offset:2048
	ds_read_b128 v[102:105], v102 offset:3072
	ds_read_b128 v[106:109], v118
	ds_read_b128 v[110:113], v118 offset:1024
	ds_read_b128 v[114:117], v118 offset:2048
	ds_read_b128 v[118:121], v118 offset:3072
	s_mov_b32 m0, s66
	v_lshl_add_u64 v[238:239], s[48:49], 0, v[8:9]
	ds_read_b128 v[158:161], v85 offset:32768
	ds_read_b128 v[170:173], v85 offset:33792
	ds_read_b128 v[186:189], v85 offset:34816
	ds_read_b128 v[190:193], v85 offset:35840
	ds_read_b128 v[196:199], v85 offset:36864
	ds_read_b128 v[200:203], v85 offset:37888
	ds_read_b128 v[208:211], v85 offset:38912
	ds_read_b128 v[228:231], v85 offset:39936
	global_load_lds_dwordx4 v[238:239], off
	v_lshl_add_u64 v[238:239], s[48:49], 0, v[78:79]
	s_mov_b32 m0, s67
	s_nop 0
	global_load_lds_dwordx4 v[238:239], off
	s_waitcnt vmcnt(8)
	s_waitcnt lgkmcnt(0)
	s_barrier
	s_setprio 1
	v_mfma_f32_16x16x32_bf16 v[182:185], v[90:93], v[158:161], v[182:185]
	v_mfma_f32_16x16x32_bf16 v[178:181], v[98:101], v[158:161], v[178:181]
	v_mfma_f32_16x16x32_bf16 v[166:169], v[90:93], v[186:189], v[166:169]
	v_mfma_f32_16x16x32_bf16 v[162:165], v[98:101], v[186:189], v[162:165]
	v_mfma_f32_16x16x32_bf16 v[150:153], v[90:93], v[196:199], v[150:153]
	v_mfma_f32_16x16x32_bf16 v[146:149], v[98:101], v[196:199], v[146:149]
	v_mfma_f32_16x16x32_bf16 v[126:129], v[90:93], v[208:211], v[126:129]
	v_mfma_f32_16x16x32_bf16 v[122:125], v[98:101], v[208:211], v[122:125]
	v_mfma_f32_16x16x32_bf16 v[182:185], v[94:97], v[170:173], v[182:185]
	v_mfma_f32_16x16x32_bf16 v[178:181], v[102:105], v[170:173], v[178:181]
	v_mfma_f32_16x16x32_bf16 v[166:169], v[94:97], v[190:193], v[166:169]
	v_mfma_f32_16x16x32_bf16 v[162:165], v[102:105], v[190:193], v[162:165]
	v_mfma_f32_16x16x32_bf16 v[150:153], v[94:97], v[200:203], v[150:153]
	v_mfma_f32_16x16x32_bf16 v[146:149], v[102:105], v[200:203], v[146:149]
	v_mfma_f32_16x16x32_bf16 v[126:129], v[94:97], v[228:231], v[126:129]
	v_mfma_f32_16x16x32_bf16 v[122:125], v[102:105], v[228:231], v[122:125]
	s_setprio 0
	s_setprio 1
	v_mfma_f32_16x16x32_bf16 v[174:177], v[106:109], v[158:161], v[174:177]
	v_mfma_f32_16x16x32_bf16 v[130:133], v[114:117], v[158:161], v[130:133]
	v_mfma_f32_16x16x32_bf16 v[174:177], v[110:113], v[170:173], v[174:177]
	v_mfma_f32_16x16x32_bf16 v[170:173], v[118:121], v[170:173], v[130:133]
	v_mfma_f32_16x16x32_bf16 v[130:133], v[106:109], v[186:189], v[134:137]
	v_mfma_f32_16x16x32_bf16 v[158:161], v[110:113], v[190:193], v[130:133]
	v_mfma_f32_16x16x32_bf16 v[130:133], v[114:117], v[186:189], v[154:157]
	v_mfma_f32_16x16x32_bf16 v[154:157], v[118:121], v[190:193], v[130:133]
	v_mfma_f32_16x16x32_bf16 v[130:133], v[106:109], v[196:199], v[142:145]
	v_mfma_f32_16x16x32_bf16 v[142:145], v[110:113], v[200:203], v[130:133]
	v_mfma_f32_16x16x32_bf16 v[130:133], v[114:117], v[196:199], v[138:141]
	v_mfma_f32_16x16x32_bf16 v[86:89], v[106:109], v[208:211], v[86:89]
	v_mfma_f32_16x16x32_bf16 v[74:77], v[114:117], v[208:211], v[74:77]
	v_mfma_f32_16x16x32_bf16 v[138:141], v[118:121], v[200:203], v[130:133]
	v_mfma_f32_16x16x32_bf16 v[86:89], v[110:113], v[228:231], v[86:89]
	v_mfma_f32_16x16x32_bf16 v[74:77], v[118:121], v[228:231], v[74:77]
	s_setprio 0
	s_barrier
; #define PG8_STAGE(bufoff, gbase, voff) do { _Pragma("unroll") for (int _i = 0; _i < 2; ++_i) \
;         __builtin_amdgcn_global_load_lds((const unsigned*)((const char*)(gbase) + (voff)[_i]), (LAS unsigned*)(lds + (bufoff) + ldsw + _i * 8192), 16, 0, 0); } while (0)
; #define PG8_LDA(dst, b, h) do { _Pragma("unroll") for (int m = 0; m < 4; ++m) _Pragma("unroll") for (int k = 0; k < 2; ++k) dst[m][k] = *(const LAS bf16x8*)(lds + PG8_SA(b, h) + aoff + m * 2048 + k * 1024); } while (0)
; #define PG8_MMA(ai, bj, At, Bt) do { __builtin_amdgcn_s_setprio(1); _Pragma("unroll") for (int m = 0; m < 4; ++m) _Pragma("unroll") for (int n = 0; n < 2; ++n) _Pragma("unroll") for (int k = 0; k < 2; ++k) \
;         acc[ai][bj][m][n] = __builtin_amdgcn_mfma_f32_16x16x32_bf16(Bt[n][k], At[m][k], acc[ai][bj][m][n], 0, 0, 0); __builtin_amdgcn_s_setprio(0); } while (0)
; #define PG8_WAIT_V(n) asm volatile("s_waitcnt vmcnt(" #n ")" ::: "memory")
; #define PG8_WAIT_L(n) asm volatile("s_waitcnt lgkmcnt(" #n ")" ::: "memory")
; #define PG8_BAR __builtin_amdgcn_s_barrier()
; #define PG8_SCHED __builtin_amdgcn_sched_barrier(0)
; template <class Epi, class Sched, bool GATHER = false>
; __device__ __forceinline__ void gemm_phase(LAS unsigned char* lds, const int lda, const int ldb, const int K, const Sched& S, const Epi& E, const int* gidx = nullptr) {
;     ...
;             PG8_LDA(At, 1, 1); PG8_STAGE(PG8_SB(1, 0), b3, voffB); PG8_STAGE(PG8_SB(1, 1), b3 + hstepB, voffB); PG8_STAGE(PG8_SA(1, 0), a3, o2[0]);
;             PG8_WAIT_V(8); PG8_WAIT_L(0); PG8_BAR; PG8_MMA(1, 0, At, B0); PG8_MMA(1, 1, At, B1); PG8_BAR; PG8_SCHED;
;         }
;         if (wr == 0) PG8_BAR;
	s_add_i32 s28, s28, s50
	v_lshl_add_u64 v[204:205], v[204:205], 0, s[64:65]
	s_mov_b32 m0, s28
	ds_read_b128 v[130:133], v85 offset:49152
	ds_read_b128 v[134:137], v85 offset:50176
	ds_read_b128 v[186:189], v85 offset:51200
	ds_read_b128 v[190:193], v85 offset:52224
	ds_read_b128 v[196:199], v85 offset:53248
	ds_read_b128 v[200:203], v85 offset:54272
	ds_read_b128 v[208:211], v85 offset:55296
	ds_read_b128 v[228:231], v85 offset:56320
	global_load_lds_dwordx4 v[204:205], off
	s_add_i32 m0, s28, 0x2000
	s_add_u32 s28, s34, 0x80080
	v_lshl_add_u64 v[204:205], v[232:233], 0, s[64:65]
	s_addc_u32 s29, s35, 0
	s_add_i32 s33, s33, s50
	global_load_lds_dwordx4 v[204:205], off
	v_lshl_add_u64 v[204:205], s[28:29], 0, v[194:195]
	s_mov_b32 m0, s33
	s_nop 0
	global_load_lds_dwordx4 v[204:205], off
	v_lshl_add_u64 v[204:205], s[28:29], 0, v[2:3]
	s_add_i32 m0, s33, 0x2000
	s_nop 0
	global_load_lds_dwordx4 v[204:205], off
	v_lshl_add_u64 v[204:205], v[234:235], 0, s[64:65]
	s_mov_b32 m0, s70
	s_nop 0
	global_load_lds_dwordx4 v[204:205], off
	v_lshl_add_u64 v[204:205], v[236:237], 0, s[64:65]
	s_mov_b32 m0, s71
	s_nop 0
	global_load_lds_dwordx4 v[204:205], off
	s_waitcnt vmcnt(8)
	s_waitcnt lgkmcnt(0)
	s_barrier
	s_setprio 1
	v_mfma_f32_16x16x32_bf16 v[70:73], v[90:93], v[130:133], v[70:73]
	v_mfma_f32_16x16x32_bf16 v[66:69], v[98:101], v[130:133], v[66:69]
	v_mfma_f32_16x16x32_bf16 v[54:57], v[90:93], v[186:189], v[54:57]
	v_mfma_f32_16x16x32_bf16 v[46:49], v[98:101], v[186:189], v[46:49]
	v_mfma_f32_16x16x32_bf16 v[34:37], v[90:93], v[196:199], v[34:37]
	v_mfma_f32_16x16x32_bf16 v[26:29], v[98:101], v[196:199], v[26:29]
	v_mfma_f32_16x16x32_bf16 v[22:25], v[90:93], v[208:211], v[22:25]
	v_mfma_f32_16x16x32_bf16 v[18:21], v[98:101], v[208:211], v[18:21]
	v_mfma_f32_16x16x32_bf16 v[70:73], v[94:97], v[134:137], v[70:73]
	v_mfma_f32_16x16x32_bf16 v[66:69], v[102:105], v[134:137], v[66:69]
	v_mfma_f32_16x16x32_bf16 v[54:57], v[94:97], v[190:193], v[54:57]
	v_mfma_f32_16x16x32_bf16 v[46:49], v[102:105], v[190:193], v[46:49]
	v_mfma_f32_16x16x32_bf16 v[34:37], v[94:97], v[200:203], v[34:37]
	v_mfma_f32_16x16x32_bf16 v[26:29], v[102:105], v[200:203], v[26:29]
	v_mfma_f32_16x16x32_bf16 v[22:25], v[94:97], v[228:231], v[22:25]
	v_mfma_f32_16x16x32_bf16 v[18:21], v[102:105], v[228:231], v[18:21]
	s_setprio 0
	s_setprio 1
	v_mfma_f32_16x16x32_bf16 v[62:65], v[106:109], v[130:133], v[62:65]
	v_mfma_f32_16x16x32_bf16 v[58:61], v[114:117], v[130:133], v[58:61]
	v_mfma_f32_16x16x32_bf16 v[50:53], v[106:109], v[186:189], v[50:53]
	v_mfma_f32_16x16x32_bf16 v[42:45], v[114:117], v[186:189], v[42:45]
	v_mfma_f32_16x16x32_bf16 v[38:41], v[106:109], v[196:199], v[38:41]
	v_mfma_f32_16x16x32_bf16 v[30:33], v[114:117], v[196:199], v[30:33]
	v_mfma_f32_16x16x32_bf16 v[14:17], v[106:109], v[208:211], v[14:17]
	v_mfma_f32_16x16x32_bf16 v[10:13], v[114:117], v[208:211], v[10:13]
	v_mfma_f32_16x16x32_bf16 v[62:65], v[110:113], v[134:137], v[62:65]
	v_mfma_f32_16x16x32_bf16 v[58:61], v[118:121], v[134:137], v[58:61]
	v_mfma_f32_16x16x32_bf16 v[50:53], v[110:113], v[190:193], v[50:53]
	v_mfma_f32_16x16x32_bf16 v[42:45], v[118:121], v[190:193], v[42:45]
	v_mfma_f32_16x16x32_bf16 v[38:41], v[110:113], v[200:203], v[38:41]
	v_mfma_f32_16x16x32_bf16 v[30:33], v[118:121], v[200:203], v[30:33]
	v_mfma_f32_16x16x32_bf16 v[14:17], v[110:113], v[228:231], v[14:17]
	v_mfma_f32_16x16x32_bf16 v[10:13], v[118:121], v[228:231], v[10:13]
	s_setprio 0
	s_barrier
	s_add_i32 s72, s72, 2
	s_add_u32 s12, s12, 0x100
	s_addc_u32 s13, s13, 0
	s_cmp_gt_u32 s72, 29
	s_cbranch_scc0 .LBB0_1186
	s_cmpk_lt_u32 s8, 0x100
	s_cbranch_scc0 .LBB0_1189
	s_barrier

; #define PG8_AOFF(of, u) do { _Pragma("unroll") for (int hh_ = 0; hh_ < 2; ++hh_) _Pragma("unroll") for (int i_ = 0; i_ < 2; ++i_) { \
;         if constexpr (GATHER) of[hh_][i_] = (unsigned)gidx[(u).pm * 256 + hh_ * 128 + RA[i_]] * (unsigned)(lda * 2) + CA2[i_]; \
;         else of[hh_][i_] = (unsigned)((hh_ * HALF + RA[i_]) * lda) * 2u + CA2[i_]; } } while (0)
; #define PG8_STAGE(bufoff, gbase, voff) do { _Pragma("unroll") for (int _i = 0; _i < 2; ++_i) \
;         __builtin_amdgcn_global_load_lds((const unsigned*)((const char*)(gbase) + (voff)[_i]), (LAS unsigned*)(lds + (bufoff) + ldsw + _i * 8192), 16, 0, 0); } while (0)
; #define PG8_LDA(dst, b, h) do { _Pragma("unroll") for (int m = 0; m < 4; ++m) _Pragma("unroll") for (int k = 0; k < 2; ++k) dst[m][k] = *(const LAS bf16x8*)(lds + PG8_SA(b, h) + aoff + m * 2048 + k * 1024); } while (0)
; #define PG8_LDB(dst, b, h) do { _Pragma("unroll") for (int n = 0; n < 2; ++n) _Pragma("unroll") for (int k = 0; k < 2; ++k) dst[n][k] = *(const LAS bf16x8*)(lds + PG8_SB(b, h) + boff + n * 2048 + k * 1024); } while (0)
; template <class Epi, class Sched, bool GATHER = false>
; __device__ __forceinline__ void gemm_phase(LAS unsigned char* lds, const int lda, const int ldb, const int K, const Sched& S, const Epi& E, const int* gidx = nullptr) {
;     ...
;         for (int t = 0; t < nt; t += 2) {
;             const bool last = (t == nt - 2);
;             if constexpr (GATHER) { if (last && has_next) PG8_AOFF(ofn, nxt); }
;             const char* a1 = cA + (size_t)(t + 1) * kstep;
;             const char* a2 = last ? nA : cA + (size_t)(t + 2) * kstep; const char* b2 = last ? nB : cB + (size_t)(t + 2) * kstep;
;             const char* a3 = a2 + kstep; const char* b3 = b2 + kstep;
;             unsigned o2[2][2];
; #pragma unroll
;             for (int hh = 0; hh < 2; ++hh)
; #pragma unroll
;                 for (int i = 0; i < 2; ++i) { if constexpr (GATHER) o2[hh][i] = last ? ofn[hh][i] : ofc[hh][i]; else o2[hh][i] = ofc[hh][i]; }
;             PG8_LDB(B0, 0, 0); PG8_LDB(B1, 0, 1); PG8_SCHED; PG8_LDA(At, 0, 0); PG8_STAGE(PG8_SA(1, 1), a1, ofc[1]);
;             PG8_WAIT_V(8); PG8_WAIT_L(0); PG8_BAR; PG8_MMA(0, 0, At, B0); PG8_MMA(0, 1, At, B1); PG8_BAR; PG8_SCHED;
;             PG8_LDA(At, 0, 1); PG8_STAGE(PG8_SB(0, 0), b2, voffB); PG8_STAGE(PG8_SB(0, 1), b2 + hstepB, voffB); PG8_STAGE(PG8_SA(0, 0), a2, o2[0]);
.LBB0_1666:
	s_add_i32 s28, 0, 0x10000
	v_add_u32_e32 v135, s28, v159
	s_add_i32 s33, 0, 0x14000
	ds_read_b128 v[164:167], v135
	ds_read_b128 v[168:171], v135 offset:1024
	ds_read_b128 v[172:175], v135 offset:2048
	ds_read_b128 v[176:179], v135 offset:3072
	v_add_u32_e32 v135, s33, v159
	ds_read_b128 v[180:183], v135
	ds_read_b128 v[184:187], v135 offset:1024
	ds_read_b128 v[188:191], v135 offset:2048
	ds_read_b128 v[196:199], v135 offset:3072
	v_cndmask_b32_e64 v194, v138, v141, s[34:35]
	v_cndmask_b32_e64 v192, v136, v143, s[34:35]
	v_cndmask_b32_e64 v135, v140, v161, s[34:35]
	v_cndmask_b32_e64 v137, v142, v162, s[34:35]
	v_lshl_add_u64 v[222:223], v[154:155], 0, s[44:45]
	s_add_i32 m0, s10, 0xc000
	ds_read_b128 v[200:203], v160
	ds_read_b128 v[204:207], v160 offset:1024
	ds_read_b128 v[208:211], v160 offset:2048
	ds_read_b128 v[228:231], v160 offset:3072
	ds_read_b128 v[232:235], v160 offset:4096
	ds_read_b128 v[236:239], v160 offset:5120
	ds_read_b128 v[240:243], v160 offset:6144
	ds_read_b128 v[244:247], v160 offset:7168
	s_add_u32 s12, s26, s44
	s_addc_u32 s13, s27, s45
	s_add_u32 s28, s12, 0x24400100
	s_addc_u32 s29, s13, 0
	s_and_b64 s[12:13], s[34:35], exec
	s_cselect_b32 s49, s17, s29
	s_cselect_b32 s48, s16, s28
	s_add_u32 s28, s72, s44
	s_addc_u32 s29, s73, s45
	s_and_b64 s[12:13], s[34:35], exec
	s_cselect_b32 s13, s41, s29
	s_cselect_b32 s12, s40, s28
	s_add_i32 s28, 0, 0x10000
	global_load_lds_dwordx4 v[222:223], off
	v_lshl_add_u64 v[222:223], v[152:153], 0, s[44:45]
	s_add_i32 m0, s10, 0xe000
	s_nop 0
	global_load_lds_dwordx4 v[222:223], off
	s_waitcnt vmcnt(8)
	s_waitcnt lgkmcnt(0)
	s_barrier
	s_setprio 1
	v_mfma_f32_16x16x32_bf16 v[126:129], v[164:167], v[200:203], v[126:129]
	v_mfma_f32_16x16x32_bf16 v[118:121], v[172:175], v[200:203], v[118:121]
	v_mfma_f32_16x16x32_bf16 v[110:113], v[164:167], v[208:211], v[110:113]
	v_mfma_f32_16x16x32_bf16 v[102:105], v[172:175], v[208:211], v[102:105]
	v_mfma_f32_16x16x32_bf16 v[94:97], v[164:167], v[232:235], v[94:97]
	v_mfma_f32_16x16x32_bf16 v[86:89], v[172:175], v[232:235], v[86:89]
	v_mfma_f32_16x16x32_bf16 v[78:81], v[164:167], v[240:243], v[78:81]
	v_mfma_f32_16x16x32_bf16 v[70:73], v[172:175], v[240:243], v[70:73]
	v_mfma_f32_16x16x32_bf16 v[126:129], v[168:171], v[204:207], v[126:129]
	v_mfma_f32_16x16x32_bf16 v[118:121], v[176:179], v[204:207], v[118:121]
	v_mfma_f32_16x16x32_bf16 v[110:113], v[168:171], v[228:231], v[110:113]
	v_mfma_f32_16x16x32_bf16 v[102:105], v[176:179], v[228:231], v[102:105]
	v_mfma_f32_16x16x32_bf16 v[94:97], v[168:171], v[236:239], v[94:97]
	v_mfma_f32_16x16x32_bf16 v[86:89], v[176:179], v[236:239], v[86:89]
	v_mfma_f32_16x16x32_bf16 v[78:81], v[168:171], v[244:247], v[78:81]
	v_mfma_f32_16x16x32_bf16 v[70:73], v[176:179], v[244:247], v[70:73]
	s_setprio 0
	s_setprio 1
	v_mfma_f32_16x16x32_bf16 v[122:125], v[180:183], v[200:203], v[122:125]
	v_mfma_f32_16x16x32_bf16 v[114:117], v[188:191], v[200:203], v[114:117]
	v_mfma_f32_16x16x32_bf16 v[106:109], v[180:183], v[208:211], v[106:109]
	v_mfma_f32_16x16x32_bf16 v[98:101], v[188:191], v[208:211], v[98:101]
	v_mfma_f32_16x16x32_bf16 v[90:93], v[180:183], v[232:235], v[90:93]
	v_mfma_f32_16x16x32_bf16 v[82:85], v[188:191], v[232:235], v[82:85]
	v_mfma_f32_16x16x32_bf16 v[74:77], v[180:183], v[240:243], v[74:77]
	v_mfma_f32_16x16x32_bf16 v[66:69], v[188:191], v[240:243], v[66:69]
	v_mfma_f32_16x16x32_bf16 v[122:125], v[184:187], v[204:207], v[122:125]
	v_mfma_f32_16x16x32_bf16 v[114:117], v[196:199], v[204:207], v[114:117]
	v_mfma_f32_16x16x32_bf16 v[106:109], v[184:187], v[228:231], v[106:109]
	v_mfma_f32_16x16x32_bf16 v[98:101], v[196:199], v[228:231], v[98:101]
	v_mfma_f32_16x16x32_bf16 v[90:93], v[184:187], v[236:239], v[90:93]
	v_mfma_f32_16x16x32_bf16 v[82:85], v[196:199], v[236:239], v[82:85]
	v_mfma_f32_16x16x32_bf16 v[74:77], v[184:187], v[244:247], v[74:77]
	v_mfma_f32_16x16x32_bf16 v[66:69], v[196:199], v[244:247], v[66:69]
	s_setprio 0
	s_barrier
	s_add_i32 s28, s28, s9
	v_lshl_add_u64 v[222:223], s[12:13], 0, v[130:131]
	s_mov_b32 m0, s28
	ds_read_b128 v[200:203], v160 offset:16384
	ds_read_b128 v[204:207], v160 offset:17408
	ds_read_b128 v[208:211], v160 offset:18432
	ds_read_b128 v[228:231], v160 offset:19456
	ds_read_b128 v[232:235], v160 offset:20480
	ds_read_b128 v[236:239], v160 offset:21504
	ds_read_b128 v[240:243], v160 offset:22528
	ds_read_b128 v[244:247], v160 offset:23552
	global_load_lds_dwordx4 v[222:223], off
	s_add_i32 m0, s28, 0x2000
	s_add_u32 s28, s12, 0x80000
	v_lshl_add_u64 v[224:225], s[12:13], 0, v[132:133]
	s_addc_u32 s29, s13, 0
	s_add_i32 s33, s33, s9
	global_load_lds_dwordx4 v[224:225], off
	v_lshl_add_u64 v[214:215], s[28:29], 0, v[130:131]
	s_mov_b32 m0, s33
	v_mov_b32_e32 v193, v195
	global_load_lds_dwordx4 v[214:215], off
	v_lshl_add_u64 v[214:215], s[28:29], 0, v[132:133]
	s_add_i32 m0, s33, 0x2000
	s_nop 0
	global_load_lds_dwordx4 v[214:215], off
	s_mov_b32 m0, s10
	v_lshl_add_u64 v[214:215], s[48:49], 0, v[194:195]
	global_load_lds_dwordx4 v194, s[48:49]
	s_mov_b32 m0, s11
	s_nop 0
	global_load_lds_dwordx4 v192, s[48:49]
	s_waitcnt vmcnt(8)
	s_waitcnt lgkmcnt(0)
	v_lshl_add_u64 v[192:193], s[48:49], 0, v[192:193]
	s_barrier
; #define PG8_STAGE(bufoff, gbase, voff) do { _Pragma("unroll") for (int _i = 0; _i < 2; ++_i) \
;         __builtin_amdgcn_global_load_lds((const unsigned*)((const char*)(gbase) + (voff)[_i]), (LAS unsigned*)(lds + (bufoff) + ldsw + _i * 8192), 16, 0, 0); } while (0)
; #define PG8_LDA(dst, b, h) do { _Pragma("unroll") for (int m = 0; m < 4; ++m) _Pragma("unroll") for (int k = 0; k < 2; ++k) dst[m][k] = *(const LAS bf16x8*)(lds + PG8_SA(b, h) + aoff + m * 2048 + k * 1024); } while (0)
; #define PG8_LDB(dst, b, h) do { _Pragma("unroll") for (int n = 0; n < 2; ++n) _Pragma("unroll") for (int k = 0; k < 2; ++k) dst[n][k] = *(const LAS bf16x8*)(lds + PG8_SB(b, h) + boff + n * 2048 + k * 1024); } while (0)
; #define PG8_MMA(ai, bj, At, Bt) do { __builtin_amdgcn_s_setprio(1); _Pragma("unroll") for (int m = 0; m < 4; ++m) _Pragma("unroll") for (int n = 0; n < 2; ++n) _Pragma("unroll") for (int k = 0; k < 2; ++k) \
;         acc[ai][bj][m][n] = __builtin_amdgcn_mfma_f32_16x16x32_bf16(Bt[n][k], At[m][k], acc[ai][bj][m][n], 0, 0, 0); __builtin_amdgcn_s_setprio(0); } while (0)
; #define PG8_WAIT_V(n) asm volatile("s_waitcnt vmcnt(" #n ")" ::: "memory")
; #define PG8_WAIT_L(n) asm volatile("s_waitcnt lgkmcnt(" #n ")" ::: "memory")
; #define PG8_BAR __builtin_amdgcn_s_barrier()
; #define PG8_SCHED __builtin_amdgcn_sched_barrier(0)
; template <class Epi, class Sched, bool GATHER = false>
; __device__ __forceinline__ void gemm_phase(LAS unsigned char* lds, const int lda, const int ldb, const int K, const Sched& S, const Epi& E, const int* gidx = nullptr) {
;     ...
;             PG8_WAIT_V(8); PG8_WAIT_L(0); PG8_BAR; PG8_MMA(1, 0, At, B0); PG8_MMA(1, 1, At, B1); PG8_BAR; PG8_SCHED;
;             PG8_LDB(B0, 1, 0); PG8_LDB(B1, 1, 1); PG8_SCHED; PG8_LDA(At, 1, 0); PG8_STAGE(PG8_SA(0, 1), a2, o2[1]);
;             PG8_WAIT_V(8); PG8_WAIT_L(0); PG8_BAR; PG8_MMA(0, 0, At, B0); PG8_MMA(0, 1, At, B1); PG8_BAR; PG8_SCHED;
	s_setprio 1
	v_mfma_f32_16x16x32_bf16 v[62:65], v[164:167], v[200:203], v[62:65]
	v_mfma_f32_16x16x32_bf16 v[54:57], v[172:175], v[200:203], v[54:57]
	v_mfma_f32_16x16x32_bf16 v[46:49], v[164:167], v[208:211], v[46:49]
	v_mfma_f32_16x16x32_bf16 v[38:41], v[172:175], v[208:211], v[38:41]
	v_mfma_f32_16x16x32_bf16 v[22:25], v[164:167], v[232:235], v[22:25]
	v_mfma_f32_16x16x32_bf16 v[18:21], v[172:175], v[232:235], v[18:21]
	v_mfma_f32_16x16x32_bf16 v[6:9], v[164:167], v[240:243], v[6:9]
	v_mfma_f32_16x16x32_bf16 v[2:5], v[172:175], v[240:243], v[2:5]
	v_mfma_f32_16x16x32_bf16 v[62:65], v[168:171], v[204:207], v[62:65]
	v_mfma_f32_16x16x32_bf16 v[54:57], v[176:179], v[204:207], v[54:57]
	v_mfma_f32_16x16x32_bf16 v[46:49], v[168:171], v[228:231], v[46:49]
	v_mfma_f32_16x16x32_bf16 v[38:41], v[176:179], v[228:231], v[38:41]
	v_mfma_f32_16x16x32_bf16 v[22:25], v[168:171], v[236:239], v[22:25]
	v_mfma_f32_16x16x32_bf16 v[18:21], v[176:179], v[236:239], v[18:21]
	v_mfma_f32_16x16x32_bf16 v[6:9], v[168:171], v[244:247], v[6:9]
	v_mfma_f32_16x16x32_bf16 v[2:5], v[176:179], v[244:247], v[2:5]
	s_setprio 0
	s_setprio 1
	v_mfma_f32_16x16x32_bf16 v[58:61], v[180:183], v[200:203], v[58:61]
	v_mfma_f32_16x16x32_bf16 v[50:53], v[188:191], v[200:203], v[50:53]
	v_mfma_f32_16x16x32_bf16 v[42:45], v[180:183], v[208:211], v[42:45]
	v_mfma_f32_16x16x32_bf16 v[34:37], v[188:191], v[208:211], v[34:37]
	v_mfma_f32_16x16x32_bf16 v[30:33], v[180:183], v[232:235], v[30:33]
	v_mfma_f32_16x16x32_bf16 v[26:29], v[188:191], v[232:235], v[26:29]
	v_mfma_f32_16x16x32_bf16 v[14:17], v[180:183], v[240:243], v[14:17]
	v_mfma_f32_16x16x32_bf16 v[10:13], v[188:191], v[240:243], v[10:13]
	v_mfma_f32_16x16x32_bf16 v[58:61], v[184:187], v[204:207], v[58:61]
	v_mfma_f32_16x16x32_bf16 v[50:53], v[196:199], v[204:207], v[50:53]
	v_mfma_f32_16x16x32_bf16 v[42:45], v[184:187], v[228:231], v[42:45]
	v_mfma_f32_16x16x32_bf16 v[34:37], v[196:199], v[228:231], v[34:37]
	v_mfma_f32_16x16x32_bf16 v[30:33], v[184:187], v[236:239], v[30:33]
	v_mfma_f32_16x16x32_bf16 v[26:29], v[196:199], v[236:239], v[26:29]
	v_mfma_f32_16x16x32_bf16 v[14:17], v[184:187], v[244:247], v[14:17]
	v_mfma_f32_16x16x32_bf16 v[10:13], v[196:199], v[244:247], v[10:13]
	s_setprio 0
	s_barrier
	s_add_i32 s28, 0, 0x18000
	v_add_u32_e32 v163, s28, v159
	s_add_i32 s29, 0, 0x1c000
	ds_read_b128 v[164:167], v163
	ds_read_b128 v[168:171], v163 offset:1024
	ds_read_b128 v[172:175], v163 offset:2048
	ds_read_b128 v[176:179], v163 offset:3072
	v_add_u32_e32 v163, s29, v159
	ds_read_b128 v[180:183], v163
	ds_read_b128 v[184:187], v163 offset:1024
	ds_read_b128 v[188:191], v163 offset:2048
	ds_read_b128 v[196:199], v163 offset:3072
	s_mov_b32 m0, s22
	ds_read_b128 v[200:203], v160 offset:32768
	ds_read_b128 v[204:207], v160 offset:33792
	ds_read_b128 v[208:211], v160 offset:34816
	ds_read_b128 v[228:231], v160 offset:35840
	ds_read_b128 v[232:235], v160 offset:36864
	ds_read_b128 v[236:239], v160 offset:37888
	ds_read_b128 v[240:243], v160 offset:38912
	ds_read_b128 v[244:247], v160 offset:39936
	global_load_lds_dwordx4 v135, s[48:49]
	s_mov_b32 m0, s23
	s_nop 0
	global_load_lds_dwordx4 v137, s[48:49]
	s_waitcnt vmcnt(8)
	s_waitcnt lgkmcnt(0)
	s_barrier
	s_setprio 1
	v_mfma_f32_16x16x32_bf16 v[126:129], v[164:167], v[200:203], v[126:129]
	v_mfma_f32_16x16x32_bf16 v[118:121], v[172:175], v[200:203], v[118:121]
	v_mfma_f32_16x16x32_bf16 v[110:113], v[164:167], v[208:211], v[110:113]
	v_mfma_f32_16x16x32_bf16 v[102:105], v[172:175], v[208:211], v[102:105]
	v_mfma_f32_16x16x32_bf16 v[94:97], v[164:167], v[232:235], v[94:97]
	v_mfma_f32_16x16x32_bf16 v[86:89], v[172:175], v[232:235], v[86:89]
	v_mfma_f32_16x16x32_bf16 v[78:81], v[164:167], v[240:243], v[78:81]
	v_mfma_f32_16x16x32_bf16 v[70:73], v[172:175], v[240:243], v[70:73]
	v_mfma_f32_16x16x32_bf16 v[126:129], v[168:171], v[204:207], v[126:129]
	v_mfma_f32_16x16x32_bf16 v[118:121], v[176:179], v[204:207], v[118:121]
	v_mfma_f32_16x16x32_bf16 v[110:113], v[168:171], v[228:231], v[110:113]
	v_mfma_f32_16x16x32_bf16 v[102:105], v[176:179], v[228:231], v[102:105]
	v_mfma_f32_16x16x32_bf16 v[94:97], v[168:171], v[236:239], v[94:97]
	v_mfma_f32_16x16x32_bf16 v[86:89], v[176:179], v[236:239], v[86:89]
	v_mfma_f32_16x16x32_bf16 v[78:81], v[168:171], v[244:247], v[78:81]
	v_mfma_f32_16x16x32_bf16 v[70:73], v[176:179], v[244:247], v[70:73]
	s_setprio 0
	s_setprio 1
	v_mfma_f32_16x16x32_bf16 v[122:125], v[180:183], v[200:203], v[122:125]
	v_mfma_f32_16x16x32_bf16 v[114:117], v[188:191], v[200:203], v[114:117]
	v_mfma_f32_16x16x32_bf16 v[106:109], v[180:183], v[208:211], v[106:109]
	v_mfma_f32_16x16x32_bf16 v[98:101], v[188:191], v[208:211], v[98:101]
	v_mfma_f32_16x16x32_bf16 v[90:93], v[180:183], v[232:235], v[90:93]
	v_mfma_f32_16x16x32_bf16 v[82:85], v[188:191], v[232:235], v[82:85]
	v_mfma_f32_16x16x32_bf16 v[74:77], v[180:183], v[240:243], v[74:77]
	v_mfma_f32_16x16x32_bf16 v[66:69], v[188:191], v[240:243], v[66:69]
	v_mfma_f32_16x16x32_bf16 v[122:125], v[184:187], v[204:207], v[122:125]
	v_mfma_f32_16x16x32_bf16 v[114:117], v[196:199], v[204:207], v[114:117]
	v_mfma_f32_16x16x32_bf16 v[106:109], v[184:187], v[228:231], v[106:109]
	v_mfma_f32_16x16x32_bf16 v[98:101], v[196:199], v[228:231], v[98:101]
	v_mfma_f32_16x16x32_bf16 v[90:93], v[184:187], v[236:239], v[90:93]
	v_mfma_f32_16x16x32_bf16 v[82:85], v[196:199], v[236:239], v[82:85]
	v_mfma_f32_16x16x32_bf16 v[74:77], v[184:187], v[244:247], v[74:77]
	v_mfma_f32_16x16x32_bf16 v[66:69], v[196:199], v[244:247], v[66:69]
	s_setprio 0
	s_barrier
; #define PG8_STAGE(bufoff, gbase, voff) do { _Pragma("unroll") for (int _i = 0; _i < 2; ++_i) \
;         __builtin_amdgcn_global_load_lds((const unsigned*)((const char*)(gbase) + (voff)[_i]), (LAS unsigned*)(lds + (bufoff) + ldsw + _i * 8192), 16, 0, 0); } while (0)
; #define PG8_LDA(dst, b, h) do { _Pragma("unroll") for (int m = 0; m < 4; ++m) _Pragma("unroll") for (int k = 0; k < 2; ++k) dst[m][k] = *(const LAS bf16x8*)(lds + PG8_SA(b, h) + aoff + m * 2048 + k * 1024); } while (0)
; #define PG8_MMA(ai, bj, At, Bt) do { __builtin_amdgcn_s_setprio(1); _Pragma("unroll") for (int m = 0; m < 4; ++m) _Pragma("unroll") for (int n = 0; n < 2; ++n) _Pragma("unroll") for (int k = 0; k < 2; ++k) \
;         acc[ai][bj][m][n] = __builtin_amdgcn_mfma_f32_16x16x32_bf16(Bt[n][k], At[m][k], acc[ai][bj][m][n], 0, 0, 0); __builtin_amdgcn_s_setprio(0); } while (0)
; #define PG8_WAIT_V(n) asm volatile("s_waitcnt vmcnt(" #n ")" ::: "memory")
; #define PG8_WAIT_L(n) asm volatile("s_waitcnt lgkmcnt(" #n ")" ::: "memory")
; #define PG8_BAR __builtin_amdgcn_s_barrier()
; #define PG8_SCHED __builtin_amdgcn_sched_barrier(0)
; template <class Epi, class Sched, bool GATHER = false>
; __device__ __forceinline__ void gemm_phase(LAS unsigned char* lds, const int lda, const int ldb, const int K, const Sched& S, const Epi& E, const int* gidx = nullptr) {
;     ...
;             PG8_LDA(At, 1, 1); PG8_STAGE(PG8_SB(1, 0), b3, voffB); PG8_STAGE(PG8_SB(1, 1), b3 + hstepB, voffB); PG8_STAGE(PG8_SA(1, 0), a3, o2[0]);
;             PG8_WAIT_V(8); PG8_WAIT_L(0); PG8_BAR; PG8_MMA(1, 0, At, B0); PG8_MMA(1, 1, At, B1); PG8_BAR; PG8_SCHED;
;         }
	s_add_i32 s28, s28, s9
	v_lshl_add_u64 v[222:223], v[222:223], 0, s[64:65]
	s_mov_b32 m0, s28
	ds_read_b128 v[200:203], v160 offset:49152
	ds_read_b128 v[204:207], v160 offset:50176
	ds_read_b128 v[208:211], v160 offset:51200
	ds_read_b128 v[228:231], v160 offset:52224
	ds_read_b128 v[232:235], v160 offset:53248
	ds_read_b128 v[236:239], v160 offset:54272
	ds_read_b128 v[240:243], v160 offset:55296
	ds_read_b128 v[244:247], v160 offset:56320
	global_load_lds_dwordx4 v[222:223], off
	s_add_i32 m0, s28, 0x2000
	s_add_u32 s12, s12, 0x80080
	v_lshl_add_u64 v[222:223], v[224:225], 0, s[64:65]
	s_addc_u32 s13, s13, 0
	s_add_i32 s28, s29, s9
	global_load_lds_dwordx4 v[222:223], off
	v_lshl_add_u64 v[222:223], s[12:13], 0, v[130:131]
	s_mov_b32 m0, s28
	v_lshl_add_u64 v[214:215], v[214:215], 0, s[64:65]
	global_load_lds_dwordx4 v[222:223], off
	v_lshl_add_u64 v[222:223], s[12:13], 0, v[132:133]
	s_add_i32 m0, s28, 0x2000
	v_lshl_add_u64 v[192:193], v[192:193], 0, s[64:65]
	global_load_lds_dwordx4 v[222:223], off
	s_mov_b32 m0, s50
	s_nop 0
	global_load_lds_dwordx4 v[214:215], off
	s_mov_b32 m0, s51
	s_nop 0
	global_load_lds_dwordx4 v[192:193], off
	s_waitcnt vmcnt(8)
	s_waitcnt lgkmcnt(0)
	s_barrier
	s_setprio 1
	v_mfma_f32_16x16x32_bf16 v[62:65], v[164:167], v[200:203], v[62:65]
	v_mfma_f32_16x16x32_bf16 v[54:57], v[172:175], v[200:203], v[54:57]
	v_mfma_f32_16x16x32_bf16 v[46:49], v[164:167], v[208:211], v[46:49]
	v_mfma_f32_16x16x32_bf16 v[38:41], v[172:175], v[208:211], v[38:41]
	v_mfma_f32_16x16x32_bf16 v[22:25], v[164:167], v[232:235], v[22:25]
	v_mfma_f32_16x16x32_bf16 v[18:21], v[172:175], v[232:235], v[18:21]
	v_mfma_f32_16x16x32_bf16 v[6:9], v[164:167], v[240:243], v[6:9]
	v_mfma_f32_16x16x32_bf16 v[2:5], v[172:175], v[240:243], v[2:5]
	v_mfma_f32_16x16x32_bf16 v[62:65], v[168:171], v[204:207], v[62:65]
	v_mfma_f32_16x16x32_bf16 v[54:57], v[176:179], v[204:207], v[54:57]
	v_mfma_f32_16x16x32_bf16 v[46:49], v[168:171], v[228:231], v[46:49]
	v_mfma_f32_16x16x32_bf16 v[38:41], v[176:179], v[228:231], v[38:41]
	v_mfma_f32_16x16x32_bf16 v[22:25], v[168:171], v[236:239], v[22:25]
	v_mfma_f32_16x16x32_bf16 v[18:21], v[176:179], v[236:239], v[18:21]
	v_mfma_f32_16x16x32_bf16 v[6:9], v[168:171], v[244:247], v[6:9]
	v_mfma_f32_16x16x32_bf16 v[2:5], v[176:179], v[244:247], v[2:5]
	s_setprio 0
	s_setprio 1
	v_mfma_f32_16x16x32_bf16 v[58:61], v[180:183], v[200:203], v[58:61]
	v_mfma_f32_16x16x32_bf16 v[50:53], v[188:191], v[200:203], v[50:53]
	v_mfma_f32_16x16x32_bf16 v[42:45], v[180:183], v[208:211], v[42:45]
	v_mfma_f32_16x16x32_bf16 v[34:37], v[188:191], v[208:211], v[34:37]
	v_mfma_f32_16x16x32_bf16 v[30:33], v[180:183], v[232:235], v[30:33]
	v_mfma_f32_16x16x32_bf16 v[26:29], v[188:191], v[232:235], v[26:29]
	v_mfma_f32_16x16x32_bf16 v[14:17], v[180:183], v[240:243], v[14:17]
	v_mfma_f32_16x16x32_bf16 v[10:13], v[188:191], v[240:243], v[10:13]
	v_mfma_f32_16x16x32_bf16 v[58:61], v[184:187], v[204:207], v[58:61]
	v_mfma_f32_16x16x32_bf16 v[50:53], v[196:199], v[204:207], v[50:53]
	v_mfma_f32_16x16x32_bf16 v[42:45], v[184:187], v[228:231], v[42:45]
	v_mfma_f32_16x16x32_bf16 v[34:37], v[196:199], v[228:231], v[34:37]
	v_mfma_f32_16x16x32_bf16 v[30:33], v[184:187], v[236:239], v[30:33]
	v_mfma_f32_16x16x32_bf16 v[26:29], v[196:199], v[236:239], v[26:29]
	v_mfma_f32_16x16x32_bf16 v[14:17], v[184:187], v[244:247], v[14:17]
	v_mfma_f32_16x16x32_bf16 v[10:13], v[196:199], v[244:247], v[10:13]
	s_setprio 0
	s_barrier
	s_add_i32 s74, s74, 2
	s_add_u32 s44, s44, 0x100
	s_addc_u32 s45, s45, 0
	s_cmp_gt_u32 s74, 29
	s_cbranch_scc1 .LBB0_1669

; #define PG8_AOFF(of, u) do { _Pragma("unroll") for (int hh_ = 0; hh_ < 2; ++hh_) _Pragma("unroll") for (int i_ = 0; i_ < 2; ++i_) { \
;         if constexpr (GATHER) of[hh_][i_] = (unsigned)gidx[(u).pm * 256 + hh_ * 128 + RA[i_]] * (unsigned)(lda * 2) + CA2[i_]; \
;         else of[hh_][i_] = (unsigned)((hh_ * HALF + RA[i_]) * lda) * 2u + CA2[i_]; } } while (0)
; #define PG8_STAGE(bufoff, gbase, voff) do { _Pragma("unroll") for (int _i = 0; _i < 2; ++_i) \
;         __builtin_amdgcn_global_load_lds((const unsigned*)((const char*)(gbase) + (voff)[_i]), (LAS unsigned*)(lds + (bufoff) + ldsw + _i * 8192), 16, 0, 0); } while (0)
; #define PG8_LDA(dst, b, h) do { _Pragma("unroll") for (int m = 0; m < 4; ++m) _Pragma("unroll") for (int k = 0; k < 2; ++k) dst[m][k] = *(const LAS bf16x8*)(lds + PG8_SA(b, h) + aoff + m * 2048 + k * 1024); } while (0)
; #define PG8_LDB(dst, b, h) do { _Pragma("unroll") for (int n = 0; n < 2; ++n) _Pragma("unroll") for (int k = 0; k < 2; ++k) dst[n][k] = *(const LAS bf16x8*)(lds + PG8_SB(b, h) + boff + n * 2048 + k * 1024); } while (0)
; template <class Epi, class Sched, bool GATHER = false>
; __device__ __forceinline__ void gemm_phase(LAS unsigned char* lds, const int lda, const int ldb, const int K, const Sched& S, const Epi& E, const int* gidx = nullptr) {
;     ...
;         for (int t = 0; t < nt; t += 2) {
;             const bool last = (t == nt - 2);
;             if constexpr (GATHER) { if (last && has_next) PG8_AOFF(ofn, nxt); }
;             const char* a1 = cA + (size_t)(t + 1) * kstep;
;             const char* a2 = last ? nA : cA + (size_t)(t + 2) * kstep; const char* b2 = last ? nB : cB + (size_t)(t + 2) * kstep;
;             const char* a3 = a2 + kstep; const char* b3 = b2 + kstep;
;             unsigned o2[2][2];
; #pragma unroll
;             for (int hh = 0; hh < 2; ++hh)
; #pragma unroll
;                 for (int i = 0; i < 2; ++i) { if constexpr (GATHER) o2[hh][i] = last ? ofn[hh][i] : ofc[hh][i]; else o2[hh][i] = ofc[hh][i]; }
;             PG8_LDB(B0, 0, 0); PG8_LDB(B1, 0, 1); PG8_SCHED; PG8_LDA(At, 0, 0); PG8_STAGE(PG8_SA(1, 1), a1, ofc[1]);
;             PG8_WAIT_V(8); PG8_WAIT_L(0); PG8_BAR; PG8_MMA(0, 0, At, B0); PG8_MMA(0, 1, At, B1); PG8_BAR; PG8_SCHED;
;             PG8_LDA(At, 0, 1); PG8_STAGE(PG8_SB(0, 0), b2, voffB); PG8_STAGE(PG8_SB(0, 1), b2 + hstepB, voffB); PG8_STAGE(PG8_SA(0, 0), a2, o2[0]);
.LBB0_1733:
	s_add_i32 s28, 0, 0x10000
	v_add_u32_e32 v146, s28, v147
	s_add_i32 s33, 0, 0x14000
	ds_read_b128 v[152:155], v146
	ds_read_b128 v[156:159], v146 offset:1024
	ds_read_b128 v[160:163], v146 offset:2048
	ds_read_b128 v[164:167], v146 offset:3072
	v_add_u32_e32 v146, s33, v147
	ds_read_b128 v[168:171], v146
	ds_read_b128 v[172:175], v146 offset:1024
	ds_read_b128 v[176:179], v146 offset:2048
	ds_read_b128 v[180:183], v146 offset:3072
	v_lshl_add_u64 v[148:149], s[44:45], 0, v[144:145]
	s_add_i32 m0, s10, 0xc000
	ds_read_b128 v[184:187], v151
	ds_read_b128 v[188:191], v151 offset:1024
	ds_read_b128 v[196:199], v151 offset:2048
	ds_read_b128 v[200:203], v151 offset:3072
	ds_read_b128 v[204:207], v151 offset:4096
	ds_read_b128 v[208:211], v151 offset:5120
	ds_read_b128 v[228:231], v151 offset:6144
	ds_read_b128 v[232:235], v151 offset:7168
	s_add_u32 s12, s44, 0x80
	s_addc_u32 s13, s45, 0
	s_cmp_eq_u32 s72, 12
	s_cselect_b32 s49, s39, s13
	s_cselect_b32 s48, s38, s12
	s_cselect_b32 s13, s41, s71
	s_cselect_b32 s12, s40, s70
	global_load_lds_dwordx4 v[148:149], off
	v_lshl_add_u64 v[148:149], s[44:45], 0, v[142:143]
	s_add_i32 m0, s10, 0xe000
	s_nop 0
	global_load_lds_dwordx4 v[148:149], off
	s_waitcnt vmcnt(8)
	s_waitcnt lgkmcnt(0)
	s_barrier
	s_setprio 1
	v_mfma_f32_16x16x32_bf16 v[126:129], v[152:155], v[184:187], v[126:129]
	v_mfma_f32_16x16x32_bf16 v[122:125], v[160:163], v[184:187], v[122:125]
	v_mfma_f32_16x16x32_bf16 v[110:113], v[152:155], v[196:199], v[110:113]
	v_mfma_f32_16x16x32_bf16 v[106:109], v[160:163], v[196:199], v[106:109]
	v_mfma_f32_16x16x32_bf16 v[94:97], v[152:155], v[204:207], v[94:97]
	v_mfma_f32_16x16x32_bf16 v[90:93], v[160:163], v[204:207], v[90:93]
	v_mfma_f32_16x16x32_bf16 v[82:85], v[152:155], v[228:231], v[82:85]
	v_mfma_f32_16x16x32_bf16 v[74:77], v[160:163], v[228:231], v[74:77]
	v_mfma_f32_16x16x32_bf16 v[126:129], v[156:159], v[188:191], v[126:129]
	v_mfma_f32_16x16x32_bf16 v[122:125], v[164:167], v[188:191], v[122:125]
	v_mfma_f32_16x16x32_bf16 v[110:113], v[156:159], v[200:203], v[110:113]
	v_mfma_f32_16x16x32_bf16 v[106:109], v[164:167], v[200:203], v[106:109]
	v_mfma_f32_16x16x32_bf16 v[94:97], v[156:159], v[208:211], v[94:97]
	v_mfma_f32_16x16x32_bf16 v[90:93], v[164:167], v[208:211], v[90:93]
	v_mfma_f32_16x16x32_bf16 v[82:85], v[156:159], v[232:235], v[82:85]
	v_mfma_f32_16x16x32_bf16 v[74:77], v[164:167], v[232:235], v[74:77]
	s_setprio 0
	s_setprio 1
	v_mfma_f32_16x16x32_bf16 v[118:121], v[168:171], v[184:187], v[118:121]
	v_mfma_f32_16x16x32_bf16 v[114:117], v[176:179], v[184:187], v[114:117]
	v_mfma_f32_16x16x32_bf16 v[102:105], v[168:171], v[196:199], v[102:105]
	v_mfma_f32_16x16x32_bf16 v[98:101], v[176:179], v[196:199], v[98:101]
	v_mfma_f32_16x16x32_bf16 v[86:89], v[168:171], v[204:207], v[86:89]
	v_mfma_f32_16x16x32_bf16 v[78:81], v[176:179], v[204:207], v[78:81]
	v_mfma_f32_16x16x32_bf16 v[62:65], v[168:171], v[228:231], v[62:65]
	v_mfma_f32_16x16x32_bf16 v[58:61], v[176:179], v[228:231], v[58:61]
	v_mfma_f32_16x16x32_bf16 v[118:121], v[172:175], v[188:191], v[118:121]
	v_mfma_f32_16x16x32_bf16 v[114:117], v[180:183], v[188:191], v[114:117]
	v_mfma_f32_16x16x32_bf16 v[102:105], v[172:175], v[200:203], v[102:105]
	v_mfma_f32_16x16x32_bf16 v[98:101], v[180:183], v[200:203], v[98:101]
	v_mfma_f32_16x16x32_bf16 v[86:89], v[172:175], v[208:211], v[86:89]
	v_mfma_f32_16x16x32_bf16 v[78:81], v[180:183], v[208:211], v[78:81]
	v_mfma_f32_16x16x32_bf16 v[62:65], v[172:175], v[232:235], v[62:65]
	v_mfma_f32_16x16x32_bf16 v[58:61], v[180:183], v[232:235], v[58:61]
	s_setprio 0
	s_barrier
	s_add_i32 s28, s28, s9
	v_lshl_add_u64 v[148:149], s[12:13], 0, v[132:133]
	s_mov_b32 m0, s28
	ds_read_b128 v[184:187], v151 offset:16384
	ds_read_b128 v[188:191], v151 offset:17408
	ds_read_b128 v[196:199], v151 offset:18432
	ds_read_b128 v[200:203], v151 offset:19456
	ds_read_b128 v[204:207], v151 offset:20480
	ds_read_b128 v[208:211], v151 offset:21504
	ds_read_b128 v[228:231], v151 offset:22528
	ds_read_b128 v[232:235], v151 offset:23552
	global_load_lds_dwordx4 v[148:149], off
	s_add_i32 m0, s28, 0x2000
	s_add_u32 s28, s12, 0x40000
	v_lshl_add_u64 v[192:193], s[12:13], 0, v[130:131]
	s_addc_u32 s29, s13, 0
	s_add_i32 s33, s33, s9
	global_load_lds_dwordx4 v[192:193], off
	v_lshl_add_u64 v[214:215], s[28:29], 0, v[132:133]
	s_mov_b32 m0, s33
	v_lshl_add_u64 v[222:223], s[48:49], 0, v[136:137]
	global_load_lds_dwordx4 v[214:215], off
	v_lshl_add_u64 v[214:215], s[28:29], 0, v[130:131]
	s_add_i32 m0, s33, 0x2000
	s_nop 0
	global_load_lds_dwordx4 v[214:215], off
	v_lshl_add_u64 v[214:215], s[48:49], 0, v[134:135]
	s_mov_b32 m0, s10
	s_nop 0
	global_load_lds_dwordx4 v[214:215], off
	s_mov_b32 m0, s11
	s_nop 0
	global_load_lds_dwordx4 v[222:223], off
	s_waitcnt vmcnt(8)
	s_waitcnt lgkmcnt(0)
	s_barrier
; #define PG8_STAGE(bufoff, gbase, voff) do { _Pragma("unroll") for (int _i = 0; _i < 2; ++_i) \
;         __builtin_amdgcn_global_load_lds((const unsigned*)((const char*)(gbase) + (voff)[_i]), (LAS unsigned*)(lds + (bufoff) + ldsw + _i * 8192), 16, 0, 0); } while (0)
; #define PG8_LDA(dst, b, h) do { _Pragma("unroll") for (int m = 0; m < 4; ++m) _Pragma("unroll") for (int k = 0; k < 2; ++k) dst[m][k] = *(const LAS bf16x8*)(lds + PG8_SA(b, h) + aoff + m * 2048 + k * 1024); } while (0)
; #define PG8_LDB(dst, b, h) do { _Pragma("unroll") for (int n = 0; n < 2; ++n) _Pragma("unroll") for (int k = 0; k < 2; ++k) dst[n][k] = *(const LAS bf16x8*)(lds + PG8_SB(b, h) + boff + n * 2048 + k * 1024); } while (0)
; #define PG8_MMA(ai, bj, At, Bt) do { __builtin_amdgcn_s_setprio(1); _Pragma("unroll") for (int m = 0; m < 4; ++m) _Pragma("unroll") for (int n = 0; n < 2; ++n) _Pragma("unroll") for (int k = 0; k < 2; ++k) \
;         acc[ai][bj][m][n] = __builtin_amdgcn_mfma_f32_16x16x32_bf16(Bt[n][k], At[m][k], acc[ai][bj][m][n], 0, 0, 0); __builtin_amdgcn_s_setprio(0); } while (0)
; #define PG8_WAIT_V(n) asm volatile("s_waitcnt vmcnt(" #n ")" ::: "memory")
; #define PG8_WAIT_L(n) asm volatile("s_waitcnt lgkmcnt(" #n ")" ::: "memory")
; #define PG8_BAR __builtin_amdgcn_s_barrier()
; #define PG8_SCHED __builtin_amdgcn_sched_barrier(0)
; template <class Epi, class Sched, bool GATHER = false>
; __device__ __forceinline__ void gemm_phase(LAS unsigned char* lds, const int lda, const int ldb, const int K, const Sched& S, const Epi& E, const int* gidx = nullptr) {
;     ...
;             PG8_WAIT_V(8); PG8_WAIT_L(0); PG8_BAR; PG8_MMA(1, 0, At, B0); PG8_MMA(1, 1, At, B1); PG8_BAR; PG8_SCHED;
;             PG8_LDB(B0, 1, 0); PG8_LDB(B1, 1, 1); PG8_SCHED; PG8_LDA(At, 1, 0); PG8_STAGE(PG8_SA(0, 1), a2, o2[1]);
;             PG8_WAIT_V(8); PG8_WAIT_L(0); PG8_BAR; PG8_MMA(0, 0, At, B0); PG8_MMA(0, 1, At, B1); PG8_BAR; PG8_SCHED;
	s_setprio 1
	v_mfma_f32_16x16x32_bf16 v[54:57], v[152:155], v[184:187], v[54:57]
	v_mfma_f32_16x16x32_bf16 v[50:53], v[160:163], v[184:187], v[50:53]
	v_mfma_f32_16x16x32_bf16 v[30:33], v[152:155], v[196:199], v[30:33]
	v_mfma_f32_16x16x32_bf16 v[26:29], v[160:163], v[196:199], v[26:29]
	v_mfma_f32_16x16x32_bf16 v[14:17], v[152:155], v[204:207], v[14:17]
	v_mfma_f32_16x16x32_bf16 v[10:13], v[160:163], v[204:207], v[10:13]
	v_mfma_f32_16x16x32_bf16 v[6:9], v[152:155], v[228:231], v[6:9]
	v_mfma_f32_16x16x32_bf16 v[2:5], v[160:163], v[228:231], v[2:5]
	v_mfma_f32_16x16x32_bf16 v[54:57], v[156:159], v[188:191], v[54:57]
	v_mfma_f32_16x16x32_bf16 v[50:53], v[164:167], v[188:191], v[50:53]
	v_mfma_f32_16x16x32_bf16 v[30:33], v[156:159], v[200:203], v[30:33]
	v_mfma_f32_16x16x32_bf16 v[26:29], v[164:167], v[200:203], v[26:29]
	v_mfma_f32_16x16x32_bf16 v[14:17], v[156:159], v[208:211], v[14:17]
	v_mfma_f32_16x16x32_bf16 v[10:13], v[164:167], v[208:211], v[10:13]
	v_mfma_f32_16x16x32_bf16 v[6:9], v[156:159], v[232:235], v[6:9]
	v_mfma_f32_16x16x32_bf16 v[2:5], v[164:167], v[232:235], v[2:5]
	s_setprio 0
	s_setprio 1
	v_mfma_f32_16x16x32_bf16 v[66:69], v[168:171], v[184:187], v[66:69]
	v_mfma_f32_16x16x32_bf16 v[70:73], v[176:179], v[184:187], v[70:73]
	v_mfma_f32_16x16x32_bf16 v[42:45], v[168:171], v[196:199], v[42:45]
	v_mfma_f32_16x16x32_bf16 v[46:49], v[176:179], v[196:199], v[46:49]
	v_mfma_f32_16x16x32_bf16 v[34:37], v[168:171], v[204:207], v[34:37]
	v_mfma_f32_16x16x32_bf16 v[38:41], v[176:179], v[204:207], v[38:41]
	v_mfma_f32_16x16x32_bf16 v[18:21], v[168:171], v[228:231], v[18:21]
	v_mfma_f32_16x16x32_bf16 v[22:25], v[176:179], v[228:231], v[22:25]
	v_mfma_f32_16x16x32_bf16 v[66:69], v[172:175], v[188:191], v[66:69]
	v_mfma_f32_16x16x32_bf16 v[70:73], v[180:183], v[188:191], v[70:73]
	v_mfma_f32_16x16x32_bf16 v[42:45], v[172:175], v[200:203], v[42:45]
	v_mfma_f32_16x16x32_bf16 v[46:49], v[180:183], v[200:203], v[46:49]
	v_mfma_f32_16x16x32_bf16 v[34:37], v[172:175], v[208:211], v[34:37]
	v_mfma_f32_16x16x32_bf16 v[38:41], v[180:183], v[208:211], v[38:41]
	v_mfma_f32_16x16x32_bf16 v[18:21], v[172:175], v[232:235], v[18:21]
	v_mfma_f32_16x16x32_bf16 v[22:25], v[180:183], v[232:235], v[22:25]
	s_setprio 0
	s_barrier
	s_add_i32 s28, 0, 0x18000
	v_add_u32_e32 v146, s28, v147
	s_add_i32 s29, 0, 0x1c000
	ds_read_b128 v[152:155], v146
	ds_read_b128 v[156:159], v146 offset:1024
	ds_read_b128 v[160:163], v146 offset:2048
	ds_read_b128 v[164:167], v146 offset:3072
	v_add_u32_e32 v146, s29, v147
	ds_read_b128 v[168:171], v146
	ds_read_b128 v[172:175], v146 offset:1024
	ds_read_b128 v[176:179], v146 offset:2048
	ds_read_b128 v[180:183], v146 offset:3072
	s_mov_b32 m0, s22
	v_lshl_add_u64 v[224:225], s[48:49], 0, v[138:139]
	ds_read_b128 v[184:187], v151 offset:32768
	ds_read_b128 v[188:191], v151 offset:33792
	ds_read_b128 v[196:199], v151 offset:34816
	ds_read_b128 v[200:203], v151 offset:35840
	ds_read_b128 v[204:207], v151 offset:36864
	ds_read_b128 v[208:211], v151 offset:37888
	ds_read_b128 v[228:231], v151 offset:38912
	ds_read_b128 v[232:235], v151 offset:39936
	global_load_lds_dwordx4 v[224:225], off
	v_lshl_add_u64 v[224:225], s[48:49], 0, v[140:141]
	s_mov_b32 m0, s23
	s_nop 0
	global_load_lds_dwordx4 v[224:225], off
	s_waitcnt vmcnt(8)
	s_waitcnt lgkmcnt(0)
	s_barrier
	s_setprio 1
	v_mfma_f32_16x16x32_bf16 v[126:129], v[152:155], v[184:187], v[126:129]
	v_mfma_f32_16x16x32_bf16 v[122:125], v[160:163], v[184:187], v[122:125]
	v_mfma_f32_16x16x32_bf16 v[110:113], v[152:155], v[196:199], v[110:113]
	v_mfma_f32_16x16x32_bf16 v[106:109], v[160:163], v[196:199], v[106:109]
	v_mfma_f32_16x16x32_bf16 v[94:97], v[152:155], v[204:207], v[94:97]
	v_mfma_f32_16x16x32_bf16 v[90:93], v[160:163], v[204:207], v[90:93]
	v_mfma_f32_16x16x32_bf16 v[82:85], v[152:155], v[228:231], v[82:85]
	v_mfma_f32_16x16x32_bf16 v[74:77], v[160:163], v[228:231], v[74:77]
	v_mfma_f32_16x16x32_bf16 v[126:129], v[156:159], v[188:191], v[126:129]
	v_mfma_f32_16x16x32_bf16 v[122:125], v[164:167], v[188:191], v[122:125]
	v_mfma_f32_16x16x32_bf16 v[110:113], v[156:159], v[200:203], v[110:113]
	v_mfma_f32_16x16x32_bf16 v[106:109], v[164:167], v[200:203], v[106:109]
	v_mfma_f32_16x16x32_bf16 v[94:97], v[156:159], v[208:211], v[94:97]
	v_mfma_f32_16x16x32_bf16 v[90:93], v[164:167], v[208:211], v[90:93]
	v_mfma_f32_16x16x32_bf16 v[82:85], v[156:159], v[232:235], v[82:85]
	v_mfma_f32_16x16x32_bf16 v[74:77], v[164:167], v[232:235], v[74:77]
	s_setprio 0
	s_setprio 1
	v_mfma_f32_16x16x32_bf16 v[118:121], v[168:171], v[184:187], v[118:121]
	v_mfma_f32_16x16x32_bf16 v[114:117], v[176:179], v[184:187], v[114:117]
	v_mfma_f32_16x16x32_bf16 v[102:105], v[168:171], v[196:199], v[102:105]
	v_mfma_f32_16x16x32_bf16 v[98:101], v[176:179], v[196:199], v[98:101]
	v_mfma_f32_16x16x32_bf16 v[86:89], v[168:171], v[204:207], v[86:89]
	v_mfma_f32_16x16x32_bf16 v[78:81], v[176:179], v[204:207], v[78:81]
	v_mfma_f32_16x16x32_bf16 v[62:65], v[168:171], v[228:231], v[62:65]
	v_mfma_f32_16x16x32_bf16 v[58:61], v[176:179], v[228:231], v[58:61]
	v_mfma_f32_16x16x32_bf16 v[118:121], v[172:175], v[188:191], v[118:121]
	v_mfma_f32_16x16x32_bf16 v[114:117], v[180:183], v[188:191], v[114:117]
	v_mfma_f32_16x16x32_bf16 v[102:105], v[172:175], v[200:203], v[102:105]
	v_mfma_f32_16x16x32_bf16 v[98:101], v[180:183], v[200:203], v[98:101]
	v_mfma_f32_16x16x32_bf16 v[86:89], v[172:175], v[208:211], v[86:89]
	v_mfma_f32_16x16x32_bf16 v[78:81], v[180:183], v[208:211], v[78:81]
	v_mfma_f32_16x16x32_bf16 v[62:65], v[172:175], v[232:235], v[62:65]
	v_mfma_f32_16x16x32_bf16 v[58:61], v[180:183], v[232:235], v[58:61]
	s_setprio 0
	s_barrier
; #define PG8_STAGE(bufoff, gbase, voff) do { _Pragma("unroll") for (int _i = 0; _i < 2; ++_i) \
;         __builtin_amdgcn_global_load_lds((const unsigned*)((const char*)(gbase) + (voff)[_i]), (LAS unsigned*)(lds + (bufoff) + ldsw + _i * 8192), 16, 0, 0); } while (0)
; #define PG8_LDA(dst, b, h) do { _Pragma("unroll") for (int m = 0; m < 4; ++m) _Pragma("unroll") for (int k = 0; k < 2; ++k) dst[m][k] = *(const LAS bf16x8*)(lds + PG8_SA(b, h) + aoff + m * 2048 + k * 1024); } while (0)
; #define PG8_MMA(ai, bj, At, Bt) do { __builtin_amdgcn_s_setprio(1); _Pragma("unroll") for (int m = 0; m < 4; ++m) _Pragma("unroll") for (int n = 0; n < 2; ++n) _Pragma("unroll") for (int k = 0; k < 2; ++k) \
;         acc[ai][bj][m][n] = __builtin_amdgcn_mfma_f32_16x16x32_bf16(Bt[n][k], At[m][k], acc[ai][bj][m][n], 0, 0, 0); __builtin_amdgcn_s_setprio(0); } while (0)
; #define PG8_WAIT_V(n) asm volatile("s_waitcnt vmcnt(" #n ")" ::: "memory")
; #define PG8_WAIT_L(n) asm volatile("s_waitcnt lgkmcnt(" #n ")" ::: "memory")
; #define PG8_BAR __builtin_amdgcn_s_barrier()
; #define PG8_SCHED __builtin_amdgcn_sched_barrier(0)
; template <class Epi, class Sched, bool GATHER = false>
; __device__ __forceinline__ void gemm_phase(LAS unsigned char* lds, const int lda, const int ldb, const int K, const Sched& S, const Epi& E, const int* gidx = nullptr) {
;     ...
;             PG8_LDA(At, 1, 1); PG8_STAGE(PG8_SB(1, 0), b3, voffB); PG8_STAGE(PG8_SB(1, 1), b3 + hstepB, voffB); PG8_STAGE(PG8_SA(1, 0), a3, o2[0]);
;             PG8_WAIT_V(8); PG8_WAIT_L(0); PG8_BAR; PG8_MMA(1, 0, At, B0); PG8_MMA(1, 1, At, B1); PG8_BAR; PG8_SCHED;
;         }
;         if (wr == 0) PG8_BAR;
	s_add_i32 s28, s28, s9
	v_lshl_add_u64 v[148:149], v[148:149], 0, s[64:65]
	s_mov_b32 m0, s28
	ds_read_b128 v[184:187], v151 offset:49152
	ds_read_b128 v[188:191], v151 offset:50176
	ds_read_b128 v[196:199], v151 offset:51200
	ds_read_b128 v[200:203], v151 offset:52224
	ds_read_b128 v[204:207], v151 offset:53248
	ds_read_b128 v[208:211], v151 offset:54272
	ds_read_b128 v[228:231], v151 offset:55296
	ds_read_b128 v[232:235], v151 offset:56320
	global_load_lds_dwordx4 v[148:149], off
	s_add_i32 m0, s28, 0x2000
	s_add_u32 s12, s12, 0x40080
	v_lshl_add_u64 v[148:149], v[192:193], 0, s[64:65]
	s_addc_u32 s13, s13, 0
	s_add_i32 s28, s29, s9
	global_load_lds_dwordx4 v[148:149], off
	v_lshl_add_u64 v[148:149], s[12:13], 0, v[132:133]
	s_mov_b32 m0, s28
	s_nop 0
	global_load_lds_dwordx4 v[148:149], off
	v_lshl_add_u64 v[148:149], s[12:13], 0, v[130:131]
	s_add_i32 m0, s28, 0x2000
	s_nop 0
	global_load_lds_dwordx4 v[148:149], off
	v_lshl_add_u64 v[148:149], v[214:215], 0, s[64:65]
	s_mov_b32 m0, s50
	s_nop 0
	global_load_lds_dwordx4 v[148:149], off
	v_lshl_add_u64 v[148:149], v[222:223], 0, s[64:65]
	s_mov_b32 m0, s51
	s_nop 0
	global_load_lds_dwordx4 v[148:149], off
	s_waitcnt vmcnt(8)
	s_waitcnt lgkmcnt(0)
	s_barrier
	s_setprio 1
	v_mfma_f32_16x16x32_bf16 v[54:57], v[152:155], v[184:187], v[54:57]
	v_mfma_f32_16x16x32_bf16 v[50:53], v[160:163], v[184:187], v[50:53]
	v_mfma_f32_16x16x32_bf16 v[30:33], v[152:155], v[196:199], v[30:33]
	v_mfma_f32_16x16x32_bf16 v[26:29], v[160:163], v[196:199], v[26:29]
	v_mfma_f32_16x16x32_bf16 v[14:17], v[152:155], v[204:207], v[14:17]
	v_mfma_f32_16x16x32_bf16 v[10:13], v[160:163], v[204:207], v[10:13]
	v_mfma_f32_16x16x32_bf16 v[6:9], v[152:155], v[228:231], v[6:9]
	v_mfma_f32_16x16x32_bf16 v[2:5], v[160:163], v[228:231], v[2:5]
	v_mfma_f32_16x16x32_bf16 v[54:57], v[156:159], v[188:191], v[54:57]
	v_mfma_f32_16x16x32_bf16 v[50:53], v[164:167], v[188:191], v[50:53]
	v_mfma_f32_16x16x32_bf16 v[30:33], v[156:159], v[200:203], v[30:33]
	v_mfma_f32_16x16x32_bf16 v[26:29], v[164:167], v[200:203], v[26:29]
	v_mfma_f32_16x16x32_bf16 v[14:17], v[156:159], v[208:211], v[14:17]
	v_mfma_f32_16x16x32_bf16 v[10:13], v[164:167], v[208:211], v[10:13]
	v_mfma_f32_16x16x32_bf16 v[6:9], v[156:159], v[232:235], v[6:9]
	v_mfma_f32_16x16x32_bf16 v[2:5], v[164:167], v[232:235], v[2:5]
	s_setprio 0
	s_setprio 1
	v_mfma_f32_16x16x32_bf16 v[66:69], v[168:171], v[184:187], v[66:69]
	v_mfma_f32_16x16x32_bf16 v[70:73], v[176:179], v[184:187], v[70:73]
	v_mfma_f32_16x16x32_bf16 v[42:45], v[168:171], v[196:199], v[42:45]
	v_mfma_f32_16x16x32_bf16 v[46:49], v[176:179], v[196:199], v[46:49]
	v_mfma_f32_16x16x32_bf16 v[34:37], v[168:171], v[204:207], v[34:37]
	v_mfma_f32_16x16x32_bf16 v[38:41], v[176:179], v[204:207], v[38:41]
	v_mfma_f32_16x16x32_bf16 v[18:21], v[168:171], v[228:231], v[18:21]
	v_mfma_f32_16x16x32_bf16 v[22:25], v[176:179], v[228:231], v[22:25]
	v_mfma_f32_16x16x32_bf16 v[66:69], v[172:175], v[188:191], v[66:69]
	v_mfma_f32_16x16x32_bf16 v[70:73], v[180:183], v[188:191], v[70:73]
	v_mfma_f32_16x16x32_bf16 v[42:45], v[172:175], v[200:203], v[42:45]
	v_mfma_f32_16x16x32_bf16 v[46:49], v[180:183], v[200:203], v[46:49]
	v_mfma_f32_16x16x32_bf16 v[34:37], v[172:175], v[208:211], v[34:37]
	v_mfma_f32_16x16x32_bf16 v[38:41], v[180:183], v[208:211], v[38:41]
	v_mfma_f32_16x16x32_bf16 v[18:21], v[172:175], v[232:235], v[18:21]
	v_mfma_f32_16x16x32_bf16 v[22:25], v[180:183], v[232:235], v[22:25]
	s_setprio 0
	s_barrier
	s_add_i32 s72, s72, 2
	s_add_u32 s44, s44, 0x100
	s_addc_u32 s45, s45, 0
	s_add_u32 s70, s70, 0x100
	s_addc_u32 s71, s71, 0
	s_cmp_gt_u32 s72, 13
	s_cbranch_scc0 .LBB0_1733
	s_and_b64 vcc, exec, s[36:37]
	s_cbranch_vccz .LBB0_1736
	s_barrier
